# attention: Q-rope MFMA B-fragments resident in VGPRs for the whole key loop (per-lane address constants rematerialised per unit), removes 4 ds_read_b128 per tile per wave
# baseline (speedup 1.0000x reference)
.LBB0_756:
	s_and_b32 s8, s8, 7
	s_ashr_i32 s31, s30, 31
	s_mul_i32 s7, s30, 0xc00
	s_mul_hi_i32 s6, s30, 0xc00
	s_add_u32 s7, s37, s7
	s_addc_u32 s6, s38, s6
	s_mul_i32 s9, s8, 0x180
	s_add_u32 s10, s7, s9
	s_addc_u32 s11, s6, 0
	s_add_u32 s6, s39, s9
	s_addc_u32 s7, s40, 0
	s_lshl_b32 s61, s8, 7
	s_lshl_b32 s8, s8, 8
	s_add_u32 s34, s41, s8
	v_readfirstlane_b32 s9, v254
	s_addc_u32 s35, s42, 0
	s_ashr_i32 s8, s9, 6
	s_lshl_b32 s82, s8, 10
	s_mov_b32 s72, s6
	s_and_b32 s73, s7, 0xffff
	s_mov_b32 s74, 0x7ffffff0
	s_mov_b32 s75, 0x20000
	s_mov_b32 s76, s34
	s_and_b32 s77, s35, 0xffff
	s_mov_b32 s78, 0x7ffffff0
	s_mov_b32 s79, 0x20000
	v_lshl_or_b32 v2, s8, 5, v188
	v_mov_b64_e32 v[0:1], s[10:11]
	v_mad_i64_i32 v[0:1], s[10:11], v2, s46, v[0:1]
	v_ashrrev_i32_e32 v142, 4, v254
	v_mov_b32_e32 v143, 0
	v_ashrrev_i32_e32 v144, 3, v254
	v_mov_b32_e32 v145, 0
	v_add_u32_e32 v146, 32, v142
	v_mov_b32_e32 v147, 0
	v_bfe_u32 v148, v254, 5, 1
	v_lshlrev_b32_e32 v148, 4, v148
	v_mov_b32_e32 v149, 0
	v_and_b32_e32 v150, 15, v254
	v_lshlrev_b32_e32 v150, 4, v150
	v_mov_b32_e32 v151, 0
	v_and_b32_e32 v152, 7, v254
	v_lshlrev_b32_e32 v152, 4, v152
	v_mov_b32_e32 v153, 0
	v_lshl_add_u64 v[26:27], s[26:27], 0, v[142:143]
	v_lshl_add_u64 v[28:29], v[146:147], 0, s[26:27]
	v_lshl_add_u64 v[38:39], v[0:1], 0, v[148:149]
	v_lshlrev_b64 v[0:1], 11, v[26:27]
	v_lshlrev_b64 v[18:19], 11, v[28:29]
	v_lshl_add_u64 v[0:1], s[34:35], 0, v[0:1]
	v_lshl_add_u64 v[18:19], s[34:35], 0, v[18:19]
	v_lshl_add_u64 v[0:1], v[0:1], 0, v[150:151]
	v_lshl_add_u64 v[22:23], v[18:19], 0, v[150:151]
	global_load_dwordx4 v[2:5], v[38:39], off offset:256
	global_load_dwordx4 v[6:9], v[38:39], off offset:288
	global_load_dwordx4 v[10:13], v[38:39], off offset:320
	global_load_dwordx4 v[14:17], v[38:39], off offset:352
	global_load_dwordx4 v[18:21], v[0:1], off
	s_nop 0
	global_load_dwordx4 v[22:25], v[22:23], off
	v_mov_b64_e32 v[0:1], s[6:7]
	v_mad_u64_u32 v[30:31], s[10:11], v26, s46, v[0:1]
	v_mad_i32_i24 v31, v27, s46, v31
	v_lshl_add_u64 v[26:27], v[30:31], 0, v[150:151]
	v_mad_u64_u32 v[30:31], s[10:11], v28, s46, v[0:1]
	v_mad_i32_i24 v31, v29, s46, v31
	v_lshl_add_u64 v[30:31], v[30:31], 0, v[150:151]
	v_lshl_add_u64 v[34:35], s[26:27], 0, v[144:145]
	global_load_dwordx4 v[26:29], v[26:27], off
	s_nop 0
	global_load_dwordx4 v[30:33], v[30:31], off
	v_mad_u64_u32 v[36:37], s[10:11], v34, s46, v[0:1]
	v_mad_i32_i24 v37, v35, s46, v37
	v_lshl_add_u64 v[34:35], v[36:37], 0, v[152:153]
	global_load_dwordx4 v[34:37], v[34:35], off offset:256
	s_nop 0
	global_load_dwordx4 v[124:127], v[38:39], off
	global_load_dwordx4 v[120:123], v[38:39], off offset:32
	global_load_dwordx4 v[116:119], v[38:39], off offset:64
	global_load_dwordx4 v[112:115], v[38:39], off offset:96
	global_load_dwordx4 v[108:111], v[38:39], off offset:128
	global_load_dwordx4 v[104:107], v[38:39], off offset:160
	global_load_dwordx4 v[100:103], v[38:39], off offset:192
	global_load_dwordx4 v[96:99], v[38:39], off offset:224
	s_lshl_b32 s8, s8, 12
	v_add_u32_e32 v190, s8, v166
	v_add_u32_e32 v191, s47, v170
	v_add_u32_e32 v192, s47, v171
	v_add_u32_e32 v193, s47, v172
	v_add_u32_e32 v194, s47, v173
	s_and_b32 s9, s9, 0x3fffffc0
	s_lshl_b32 s9, s9, 2
	s_add_i32 s62, s9, 0
	s_add_i32 s62, s62, 0x14000
	s_mov_b32 s11, s27
	s_mov_b32 s22, s27
	s_mov_b32 s23, s27
	s_mov_b32 s8, s27
	s_mov_b32 s9, s27
	s_mov_b32 s12, s27
	s_mov_b32 s13, s27
	s_mov_b32 s14, s27
	s_mov_b32 s15, s27
	s_mov_b32 s16, s27
	s_mov_b32 s17, s27
	s_mov_b32 s18, s27
	s_mov_b32 s19, s27
	s_mov_b32 s20, s27
	s_mov_b32 s21, s27
	v_add_u32_e32 v195, 0, v168
	s_mov_b32 s64, 2
	v_mov_b32_e32 v140, 0
	v_lshrrev_b32_e32 v156, 4, v254
	v_and_b32_e32 v157, 15, v156
	v_and_b32_e32 v159, 15, v254
	v_xor_b32_e32 v157, v157, v159
	v_lshlrev_b32_e32 v157, 4, v157
	v_mad_u32_u24 v154, v156, s46, v157
	v_lshrrev_b32_e32 v156, 3, v254
	v_bfe_u32 v157, v254, 4, 3
	v_and_b32_e32 v159, 7, v254
	v_xor_b32_e32 v157, v157, v159
	v_lshlrev_b32_e32 v157, 4, v157
	v_add_u32_e32 v157, 0x100, v157
	v_mad_u32_u24 v155, v156, s46, v157
	v_and_b32_e32 v196, 3, v254
	v_lshlrev_b32_e32 v196, 4, v196
	v_bfe_u32 v156, v254, 5, 2
	v_lshl_or_b32 v196, v156, 6, v196
	v_bfe_u32 v156, v254, 2, 2
	v_lshl_or_b32 v196, v156, 11, v196
	v_bfe_u32 v156, v254, 7, 1
	v_lshl_or_b32 v196, v156, 13, v196
	v_bfe_u32 v156, v254, 4, 1
	v_lshl_or_b32 v196, v156, 14, v196
	v_bfe_u32 v156, v254, 8, 1
	v_lshl_or_b32 v196, v156, 15, v196
	v_add_u32_e32 v157, 0x12000, v195
	v_lshl_add_u32 v189, v188, 2, s62
	s_waitcnt vmcnt(16)
	ds_write_b128 v190, v[2:5]
	s_waitcnt vmcnt(15)
	ds_write_b128 v190, v[6:9] offset:1024
	s_waitcnt vmcnt(14)
	ds_write_b128 v190, v[10:13] offset:2048
	s_waitcnt vmcnt(13)
	ds_write_b128 v190, v[14:17] offset:3072
	s_waitcnt vmcnt(0)
	s_waitcnt vmcnt(12)
	ds_write_b128 v175, v[18:21]
	s_waitcnt vmcnt(11)
	ds_write_b128 v176, v[22:25]
	s_waitcnt vmcnt(10)
	ds_write_b128 v177, v[26:29] offset:32768
	s_waitcnt vmcnt(9)
	ds_write_b128 v178, v[30:33] offset:32768
	s_waitcnt vmcnt(8)
	ds_write_b128 v179, v[34:37]
	s_waitcnt lgkmcnt(0)
	s_barrier
	ds_read_b128 v[2:5], v180 offset:32768
	ds_read_b128 v[6:9], v180 offset:40960
	s_waitcnt vmcnt(7) lgkmcnt(1)
	v_mfma_f32_32x32x16_bf16 v[48:63], v[2:5], v[124:127], 0
	s_waitcnt lgkmcnt(0)
	v_mfma_f32_32x32x16_bf16 v[64:79], v[6:9], v[124:127], 0
	ds_read_b128 v[2:5], v181 offset:32768
	ds_read_b128 v[6:9], v181 offset:40960
	s_waitcnt vmcnt(6) lgkmcnt(1)
	v_mfma_f32_32x32x16_bf16 v[48:63], v[2:5], v[120:123], v[48:63]
	s_waitcnt lgkmcnt(0)
	v_mfma_f32_32x32x16_bf16 v[64:79], v[6:9], v[120:123], v[64:79]
	ds_read_b128 v[2:5], v182 offset:32768
	ds_read_b128 v[6:9], v182 offset:40960
	s_waitcnt vmcnt(5) lgkmcnt(1)
	v_mfma_f32_32x32x16_bf16 v[48:63], v[2:5], v[116:119], v[48:63]
	s_waitcnt lgkmcnt(0)
	v_mfma_f32_32x32x16_bf16 v[64:79], v[6:9], v[116:119], v[64:79]
	ds_read_b128 v[2:5], v183 offset:32768
	ds_read_b128 v[6:9], v183 offset:40960
	s_waitcnt vmcnt(4) lgkmcnt(1)
	v_mfma_f32_32x32x16_bf16 v[48:63], v[2:5], v[112:115], v[48:63]
	s_waitcnt lgkmcnt(0)
	v_mfma_f32_32x32x16_bf16 v[64:79], v[6:9], v[112:115], v[64:79]
	ds_read_b128 v[2:5], v184 offset:32768
	ds_read_b128 v[6:9], v184 offset:40960
	s_waitcnt vmcnt(3) lgkmcnt(1)
	v_mfma_f32_32x32x16_bf16 v[48:63], v[2:5], v[108:111], v[48:63]
	s_waitcnt lgkmcnt(0)
	v_mfma_f32_32x32x16_bf16 v[64:79], v[6:9], v[108:111], v[64:79]
	ds_read_b128 v[2:5], v185 offset:32768
	ds_read_b128 v[6:9], v185 offset:40960
	s_waitcnt vmcnt(2) lgkmcnt(1)
	v_mfma_f32_32x32x16_bf16 v[48:63], v[2:5], v[104:107], v[48:63]
	s_waitcnt lgkmcnt(0)
	v_mfma_f32_32x32x16_bf16 v[64:79], v[6:9], v[104:107], v[64:79]
	ds_read_b128 v[2:5], v186 offset:32768
	ds_read_b128 v[6:9], v186 offset:40960
	s_waitcnt vmcnt(1) lgkmcnt(1)
	v_mfma_f32_32x32x16_bf16 v[48:63], v[2:5], v[100:103], v[48:63]
	s_waitcnt lgkmcnt(0)
	v_mfma_f32_32x32x16_bf16 v[64:79], v[6:9], v[100:103], v[64:79]
	ds_read_b128 v[2:5], v187 offset:32768
	ds_read_b128 v[6:9], v187 offset:40960
	s_waitcnt vmcnt(0) lgkmcnt(1)
	v_mfma_f32_32x32x16_bf16 v[48:63], v[2:5], v[96:99], v[48:63]
	s_waitcnt lgkmcnt(0)
	v_mfma_f32_32x32x16_bf16 v[64:79], v[6:9], v[96:99], v[64:79]
	ds_read_b128 v[2:5], v191
	ds_read_b128 v[6:9], v190
	ds_read_b128 v[10:13], v191 offset:4096
	ds_read_b128 v[14:17], v190 offset:1024
	s_waitcnt lgkmcnt(2)
	v_mfma_f32_32x32x16_bf16 v[48:63], v[2:5], v[6:9], v[48:63]
	s_waitcnt lgkmcnt(1)
	v_mfma_f32_32x32x16_bf16 v[64:79], v[10:13], v[6:9], v[64:79]
	ds_read_b128 v[2:5], v192
	ds_read_b128 v[6:9], v192 offset:4096
	s_waitcnt lgkmcnt(1)
	v_mfma_f32_32x32x16_bf16 v[48:63], v[2:5], v[14:17], v[48:63]
	s_waitcnt lgkmcnt(0)
	v_mfma_f32_32x32x16_bf16 v[64:79], v[6:9], v[14:17], v[64:79]
	ds_read_b128 v[2:5], v193
	ds_read_b128 v[6:9], v190 offset:2048
	ds_read_b128 v[10:13], v193 offset:4096
	ds_read_b128 v[14:17], v190 offset:3072
	s_waitcnt lgkmcnt(2)
	v_mfma_f32_32x32x16_bf16 v[48:63], v[2:5], v[6:9], v[48:63]
	s_waitcnt lgkmcnt(1)
	v_mfma_f32_32x32x16_bf16 v[64:79], v[10:13], v[6:9], v[64:79]
	ds_read_b128 v[2:5], v194
	ds_read_b128 v[6:9], v194 offset:4096
	s_waitcnt lgkmcnt(1)
	v_mfma_f32_32x32x16_bf16 v[48:63], v[2:5], v[14:17], v[48:63]
	s_waitcnt lgkmcnt(0)
	v_mfma_f32_32x32x16_bf16 v[64:79], v[6:9], v[14:17], v[64:79]
	s_nop 9
	v_max_f32_e32 v2, v49, v49
	v_max_f32_e32 v3, v48, v48
	v_max_f32_e32 v2, v3, v2
	v_max3_f32 v2, v2, v50, v51
	v_max3_f32 v2, v2, v52, v53
	v_max3_f32 v2, v2, v54, v55
	v_max3_f32 v2, v2, v56, v57
	v_max3_f32 v2, v2, v58, v59
	v_max3_f32 v2, v2, v60, v61
	v_max3_f32 v2, v2, v62, v63
	v_max3_f32 v2, v2, v64, v65
	v_max3_f32 v2, v2, v66, v67
	v_max3_f32 v2, v2, v68, v69
	v_max3_f32 v2, v2, v70, v71
	v_max3_f32 v2, v2, v72, v73
	v_max3_f32 v2, v2, v74, v75
	v_max3_f32 v2, v2, v76, v77
	v_max3_f32 v2, v2, v78, v79
	v_mov_b32_e32 v3, v2
	s_nop 1
	v_permlane32_swap_b32_e32 v2, v3
	v_max_f32_e32 v3, v3, v3
	v_max_f32_e32 v2, v2, v2
	v_max_f32_e32 v2, v2, v3
	v_add_f32_e32 v3, 0x7149f2ca, v2
	v_cmp_ge_f32_e32 vcc, s48, v3
	s_cmp_eq_u64 vcc, exec
	s_cselect_b64 vcc, -1, 0
	s_add_i32 s10, s26, 64
	v_max_f32_e32 v128, 0xf149f2ca, v2
	v_lshl_add_u64 v[2:3], s[10:11], 0, v[142:143]
	v_lshl_add_u64 v[4:5], v[146:147], 0, s[10:11]
	v_lshl_add_u64 v[6:7], s[10:11], 0, v[144:145]
	v_lshlrev_b64 v[8:9], 11, v[2:3]
	v_lshlrev_b64 v[10:11], 11, v[4:5]
	v_mad_u64_u32 v[12:13], s[10:11], v2, s46, v[0:1]
	v_mad_u64_u32 v[14:15], s[10:11], v4, s46, v[0:1]
	v_mad_u64_u32 v[0:1], s[10:11], v6, s46, v[0:1]
	v_lshl_add_u64 v[8:9], s[34:35], 0, v[8:9]
	v_lshl_add_u64 v[10:11], s[34:35], 0, v[10:11]
	v_mad_i32_i24 v13, v3, s46, v13
	v_mad_i32_i24 v15, v5, s46, v15
	v_mad_i32_i24 v1, v7, s46, v1
	v_lshl_add_u64 v[2:3], v[8:9], 0, v[150:151]
	v_lshl_add_u64 v[4:5], v[10:11], 0, v[150:151]
	v_lshl_add_u64 v[6:7], v[12:13], 0, v[150:151]
	v_lshl_add_u64 v[8:9], v[14:15], 0, v[150:151]
	v_lshl_add_u64 v[0:1], v[0:1], 0, v[152:153]
	global_load_dwordx4 v[80:83], v[2:3], off
	global_load_dwordx4 v[84:87], v[4:5], off
	global_load_dwordx4 v[88:91], v[6:7], off
	global_load_dwordx4 v[92:95], v[8:9], off
	global_load_dwordx4 v[200:203], v[0:1], off offset:256
	v_sub_f32_e32 v129, 0xf149f2ca, v128
	v_mul_f32_e32 v129, 0x3dd53b94, v129
	v_exp_f32_e32 v164, v129
	v_mov_b32_e32 v129, 0xf149f2ca
	v_cndmask_b32_e32 v198, v128, v129, vcc
	v_mul_f32_e32 v138, 0xbdd53b94, v198
	v_mov_b32_e32 v165, v138
	v_fmamk_f32 v48, v48, 0x3dd53b94, v138
	v_fmamk_f32 v49, v49, 0x3dd53b94, v138
	v_fmamk_f32 v50, v50, 0x3dd53b94, v138
	v_fmamk_f32 v51, v51, 0x3dd53b94, v138
	v_fmamk_f32 v52, v52, 0x3dd53b94, v138
	v_fmamk_f32 v53, v53, 0x3dd53b94, v138
	v_fmamk_f32 v54, v54, 0x3dd53b94, v138
	v_fmamk_f32 v55, v55, 0x3dd53b94, v138
	v_fmamk_f32 v56, v56, 0x3dd53b94, v138
	v_fmamk_f32 v57, v57, 0x3dd53b94, v138
	v_fmamk_f32 v58, v58, 0x3dd53b94, v138
	v_fmamk_f32 v59, v59, 0x3dd53b94, v138
	v_fmamk_f32 v60, v60, 0x3dd53b94, v138
	v_fmamk_f32 v61, v61, 0x3dd53b94, v138
	v_fmamk_f32 v62, v62, 0x3dd53b94, v138
	v_fmac_f32_e32 v165, 0x3dd53b94, v63
	s_mov_b32 s10, s27
	s_mov_b32 s11, s27
	v_mov_b64_e32 v[30:31], s[22:23]
	v_exp_f32_e32 v222, v48
	v_exp_f32_e32 v224, v49
	v_exp_f32_e32 v220, v50
	v_exp_f32_e32 v223, v51
	v_exp_f32_e32 v219, v52
	v_exp_f32_e32 v221, v53
	v_exp_f32_e32 v217, v54
	v_exp_f32_e32 v218, v55
	v_exp_f32_e32 v212, v56
	v_exp_f32_e32 v214, v57
	v_exp_f32_e32 v211, v58
	v_exp_f32_e32 v213, v59
	v_exp_f32_e32 v208, v60
	v_exp_f32_e32 v210, v61
	v_exp_f32_e32 v207, v62
	v_exp_f32_e32 v209, v165
	v_mov_b64_e32 v[16:17], s[8:9]
	s_waitcnt vmcnt(0)
	v_mov_b64_e32 v[28:29], s[20:21]
	v_mov_b64_e32 v[26:27], s[18:19]
	v_mov_b64_e32 v[24:25], s[16:17]
	v_mov_b64_e32 v[22:23], s[14:15]
	v_mov_b64_e32 v[20:21], s[12:13]
	v_mov_b64_e32 v[18:19], s[10:11]
	v_mov_b64_e32 v[46:47], v[30:31]
	v_mov_b64_e32 v[0:1], v[16:17]
	v_mov_b64_e32 v[62:63], v[30:31]
	v_mov_b64_e32 v[44:45], v[28:29]
	v_mov_b64_e32 v[42:43], v[26:27]
	v_mov_b64_e32 v[40:41], v[24:25]
	v_mov_b64_e32 v[38:39], v[22:23]
	v_mov_b64_e32 v[36:37], v[20:21]
	v_mov_b64_e32 v[34:35], v[18:19]
	v_mov_b64_e32 v[32:33], v[16:17]
	v_mov_b64_e32 v[2:3], v[18:19]
	v_mov_b64_e32 v[4:5], v[20:21]
	v_mov_b64_e32 v[6:7], v[22:23]
	v_mov_b64_e32 v[8:9], v[24:25]
	v_mov_b64_e32 v[10:11], v[26:27]
	v_mov_b64_e32 v[12:13], v[28:29]
	v_mov_b64_e32 v[14:15], v[30:31]
	s_add_i32 s10, s26, 0x80
	s_add_i32 s83, s26, 64
	s_sub_i32 s11, s65, 64
	v_pk_fma_f32 v[134:135], v[78:79], s[28:29], v[138:139] op_sel_hi:[1,0,0]
	v_pk_fma_f32 v[160:161], v[76:77], s[28:29], v[138:139] op_sel_hi:[1,0,0]
	v_pk_fma_f32 v[162:163], v[74:75], s[28:29], v[138:139] op_sel_hi:[1,0,0]
	v_pk_fma_f32 v[128:129], v[72:73], s[28:29], v[138:139] op_sel_hi:[1,0,0]
	v_pk_fma_f32 v[130:131], v[70:71], s[28:29], v[138:139] op_sel_hi:[1,0,0]
	v_pk_fma_f32 v[132:133], v[68:69], s[28:29], v[138:139] op_sel_hi:[1,0,0]
	v_pk_fma_f32 v[136:137], v[66:67], s[28:29], v[138:139] op_sel_hi:[1,0,0]
	v_pk_fma_f32 v[138:139], v[64:65], s[28:29], v[138:139] op_sel_hi:[1,0,0]
	v_cndmask_b32_e64 v197, v164, 1.0, vcc
	v_mov_b64_e32 v[60:61], v[28:29]
	v_mov_b64_e32 v[58:59], v[26:27]
	v_mov_b64_e32 v[56:57], v[24:25]
	v_mov_b64_e32 v[54:55], v[22:23]
	v_mov_b64_e32 v[52:53], v[20:21]
	v_mov_b64_e32 v[50:51], v[18:19]
	v_mov_b64_e32 v[48:49], v[16:17]
	s_waitcnt vmcnt(4)
	ds_write_b128 v175, v[80:83] offset:16384
	s_waitcnt vmcnt(3)
	ds_write_b128 v176, v[84:87] offset:16384
	s_waitcnt vmcnt(2)
	ds_write_b128 v177, v[88:91] offset:49152
	s_waitcnt vmcnt(1)
	ds_write_b128 v178, v[92:95] offset:49152
	s_waitcnt vmcnt(0)
	ds_write_b128 v157, v[200:203]
	ds_read_b128 v[142:145], v190
	ds_read_b128 v[146:149], v190 offset:1024
	ds_read_b128 v[150:153], v190 offset:2048
	ds_read_b128 v[156:159], v190 offset:3072
	s_waitcnt lgkmcnt(0)
	s_barrier
.LBB0_757:
	s_add_i32 s12, s64, -1
	s_sub_i32 s80, s11, 64
	s_cmp_lt_u32 s12, 3
	s_cselect_b32 s80, s10, s80
	s_mul_i32 s81, s80, 0xc00
	s_add_i32 s85, s82, 0x8000
	s_mov_b32 m0, s85
	s_add_i32 s85, s82, 0x10000
	buffer_load_dwordx4 v154, s[72:75], s81 offen lds
	s_mov_b32 m0, s85
	s_add_i32 s85, s82, 0xa000
	buffer_load_dwordx4 v155, s[72:75], s81 offen lds
	s_mov_b32 m0, s85
	s_add_i32 s81, s81, 0x18000
	buffer_load_dwordx4 v154, s[72:75], s81 offen lds
	s_lshl_b32 s81, s83, 11
	s_add_i32 s85, s82, 0x4000
	s_mov_b32 m0, s85
	s_add_i32 s85, s82, 0x6000
	buffer_load_dwordx4 v196, s[76:79], s81 offen lds
	s_mov_b32 m0, s85
	s_add_i32 s81, s81, 0x10000
	buffer_load_dwordx4 v196, s[76:79], s81 offen lds
	s_mov_b32 s84, s80
	s_add_i32 s6, 0, 0x12000
	v_add_u32_e32 v199, s6, v170
	v_add_u32_e32 v204, s6, v171
	v_add_u32_e32 v205, s6, v172
	ds_read_b128 v[64:67], v180 offset:49152
	ds_read_b128 v[68:71], v180 offset:57344
	ds_read_b128 v[200:203], v181 offset:49152
	ds_read_b128 v[226:229], v181 offset:57344
	ds_read_b128 v[230:233], v182 offset:49152
	ds_read_b128 v[234:237], v182 offset:57344
	ds_read_b128 v[238:241], v183 offset:49152
	ds_read_b128 v[242:245], v183 offset:57344
	s_waitcnt lgkmcnt(7)
	v_mfma_f32_32x32x16_bf16 v[80:95], v[64:67], v[124:127], 0
	v_exp_f32_e32 v216, v128
	v_add_f32_e32 v128, 0, v222
	v_add_f32_e32 v128, v224, v128
	v_add_f32_e32 v128, v220, v128
	v_add_f32_e32 v128, v223, v128
	v_add_f32_e32 v128, v219, v128
	v_add_f32_e32 v128, v221, v128
	s_waitcnt lgkmcnt(6)
	v_mfma_f32_32x32x16_bf16 v[64:79], v[68:71], v[124:127], 0
	v_add_f32_e32 v128, v217, v128
	v_add_f32_e32 v128, v218, v128
	v_add_f32_e32 v128, v212, v128
	v_add_f32_e32 v128, v214, v128
	v_add_f32_e32 v128, v211, v128
	v_add_f32_e32 v128, v213, v128
	v_exp_f32_e32 v138, v138
	s_waitcnt lgkmcnt(5)
	v_mfma_f32_32x32x16_bf16 v[80:95], v[200:203], v[120:123], v[80:95]
	v_add_f32_e32 v128, v208, v128
	v_exp_f32_e32 v139, v139
	v_add_f32_e32 v128, v210, v128
	v_exp_f32_e32 v164, v136
	v_add_f32_e32 v128, v207, v128
	v_exp_f32_e32 v137, v137
	v_add_f32_e32 v128, v209, v128
	s_waitcnt lgkmcnt(4)
	v_mfma_f32_32x32x16_bf16 v[64:79], v[226:229], v[120:123], v[64:79]
	ds_read_b128 v[200:203], v184 offset:49152
	ds_read_b128 v[226:229], v184 offset:57344
	v_exp_f32_e32 v165, v132
	v_add_f32_e32 v128, v138, v128
	v_add_f32_e32 v128, v139, v128
	v_exp_f32_e32 v206, v130
	v_add_f32_e32 v128, v164, v128
	v_exp_f32_e32 v215, v131
	s_waitcnt lgkmcnt(5)
	v_mfma_f32_32x32x16_bf16 v[80:95], v[230:233], v[116:119], v[80:95]
	v_add_f32_e32 v128, v137, v128
	v_add_f32_e32 v128, v165, v128
	v_exp_f32_e32 v225, v129
	v_exp_f32_e32 v162, v162
	v_exp_f32_e32 v163, v163
	v_exp_f32_e32 v160, v160
	v_exp_f32_e32 v161, v161
	s_waitcnt lgkmcnt(4)
	v_mfma_f32_32x32x16_bf16 v[64:79], v[234:237], v[116:119], v[64:79]
	ds_read_b128 v[230:233], v185 offset:49152
	ds_read_b128 v[234:237], v185 offset:57344
	v_cvt_pk_bf16_f32 v129, v220, v223
	v_cvt_pk_bf16_f32 v130, v219, v221
	v_cvt_pk_bf16_f32 v131, v217, v218
	v_cvt_pk_bf16_f32 v132, v212, v214
	v_cvt_pk_bf16_f32 v136, v138, v139
	v_cvt_pk_bf16_f32 v137, v164, v137
	s_waitcnt lgkmcnt(5)
	v_mfma_f32_32x32x16_bf16 v[80:95], v[238:241], v[112:115], v[80:95]
	v_cvt_pk_bf16_f32 v139, v206, v215
	v_permlane32_swap_b32_e32 v129, v131
	s_nop 0
	v_permlane32_swap_b32_e32 v137, v139
	s_waitcnt lgkmcnt(4)
	v_mfma_f32_32x32x16_bf16 v[64:79], v[242:245], v[112:115], v[64:79]
	ds_read_b128 v[238:241], v186 offset:49152
	ds_read_b128 v[242:245], v186 offset:57344
	s_waitcnt lgkmcnt(5)
	v_mfma_f32_32x32x16_bf16 v[80:95], v[200:203], v[108:111], v[80:95]
	s_waitcnt lgkmcnt(4)
	v_mfma_f32_32x32x16_bf16 v[64:79], v[226:229], v[108:111], v[64:79]
	ds_read_b128 v[200:203], v187 offset:49152
	ds_read_b128 v[226:229], v187 offset:57344
	s_waitcnt lgkmcnt(5)
	v_mfma_f32_32x32x16_bf16 v[80:95], v[230:233], v[104:107], v[80:95]
	s_waitcnt lgkmcnt(4)
	v_mfma_f32_32x32x16_bf16 v[64:79], v[234:237], v[104:107], v[64:79]
	ds_read_b128 v[230:233], v199
	ds_read_b128 v[234:237], v199 offset:4096
	s_waitcnt lgkmcnt(5)
	v_mfma_f32_32x32x16_bf16 v[80:95], v[238:241], v[100:103], v[80:95]
	s_waitcnt lgkmcnt(4)
	v_mfma_f32_32x32x16_bf16 v[64:79], v[242:245], v[100:103], v[64:79]
	ds_read_b128 v[238:241], v204
	ds_read_b128 v[242:245], v204 offset:4096
	v_add_u32_e32 v204, s6, v173
	s_waitcnt lgkmcnt(5)
	v_mfma_f32_32x32x16_bf16 v[80:95], v[200:203], v[96:99], v[80:95]
	s_waitcnt lgkmcnt(4)
	v_mfma_f32_32x32x16_bf16 v[64:79], v[226:229], v[96:99], v[64:79]
	ds_read_b128 v[200:203], v205
	ds_read_b128 v[226:229], v205 offset:4096
	s_waitcnt lgkmcnt(5)
	v_mfma_f32_32x32x16_bf16 v[80:95], v[230:233], v[142:145], v[80:95]
	s_waitcnt lgkmcnt(4)
	v_mfma_f32_32x32x16_bf16 v[64:79], v[234:237], v[142:145], v[64:79]
	ds_read_b128 v[230:233], v204
	ds_read_b128 v[234:237], v204 offset:4096
	s_waitcnt lgkmcnt(5)
	v_mfma_f32_32x32x16_bf16 v[80:95], v[238:241], v[146:149], v[80:95]
	s_waitcnt lgkmcnt(4)
	v_mfma_f32_32x32x16_bf16 v[64:79], v[242:245], v[146:149], v[64:79]
	s_waitcnt lgkmcnt(3)
	v_mfma_f32_32x32x16_bf16 v[80:95], v[200:203], v[150:153], v[80:95]
	v_exp_f32_e32 v205, v133
	v_cvt_pk_bf16_f32 v133, v211, v213
	v_cvt_pk_bf16_f32 v138, v165, v205
	v_add_f32_e32 v128, v205, v128
	v_add_f32_e32 v128, v206, v128
	v_add_f32_e32 v128, v215, v128
	s_waitcnt lgkmcnt(2)
	v_mfma_f32_32x32x16_bf16 v[64:79], v[226:229], v[150:153], v[64:79]
	v_add_f32_e32 v128, v216, v128
	v_add_f32_e32 v128, v225, v128
	v_add_f32_e32 v128, v162, v128
	v_add_f32_e32 v128, v163, v128
	v_add_f32_e32 v128, v160, v128
	v_add_f32_e32 v128, v161, v128
	s_waitcnt lgkmcnt(1)
	v_mfma_f32_32x32x16_bf16 v[80:95], v[230:233], v[156:159], v[80:95]
	v_exp_f32_e32 v226, v134
	v_exp_f32_e32 v227, v135
	v_cvt_pk_bf16_f32 v134, v208, v210
	v_cvt_pk_bf16_f32 v135, v207, v209
	v_add_f32_e32 v128, v226, v128
	v_add_f32_e32 v203, v227, v128
	v_mov_b32_e32 v204, v203
	s_waitcnt lgkmcnt(0)
	v_mfma_f32_32x32x16_bf16 v[64:79], v[234:237], v[156:159], v[64:79]
	s_nop 0
	v_permlane32_swap_b32_e32 v203, v204
	v_cvt_pk_bf16_f32 v128, v222, v224
	v_cvt_pk_bf16_f32 v208, v216, v225
	v_cvt_pk_bf16_f32 v209, v162, v163
	v_cvt_pk_bf16_f32 v210, v160, v161
	v_cvt_pk_bf16_f32 v211, v226, v227
	v_permlane32_swap_b32_e32 v132, v134
	v_permlane32_swap_b32_e32 v128, v130
	v_permlane32_swap_b32_e32 v133, v135
	v_permlane32_swap_b32_e32 v136, v138
	v_permlane32_swap_b32_e32 v208, v210
	v_permlane32_swap_b32_e32 v209, v211
	ds_read_b64_tr_b16 v[160:161], v167 offset:0
	ds_read_b64_tr_b16 v[162:163], v167 offset:0x800
	ds_read_b64_tr_b16 v[232:233], v167 offset:0x1000
	ds_read_b64_tr_b16 v[234:235], v167 offset:0x1800
	ds_read_b64_tr_b16 v[236:237], v167 offset:0x2000
	ds_read_b64_tr_b16 v[238:239], v167 offset:0x2800
	ds_read_b64_tr_b16 v[240:241], v167 offset:0x3000
	ds_read_b64_tr_b16 v[242:243], v167 offset:0x3800
	v_max_f32_e32 v164, v81, v81
	v_max_f32_e32 v165, v80, v80
	v_max_f32_e32 v164, v165, v164
	v_max3_f32 v164, v164, v82, v83
	v_max3_f32 v164, v164, v84, v85
	v_max3_f32 v164, v164, v86, v87
	v_max3_f32 v164, v164, v88, v89
	v_max3_f32 v164, v164, v90, v91
	v_max3_f32 v164, v164, v92, v93
	v_max3_f32 v164, v164, v94, v95
	s_waitcnt lgkmcnt(0)
	v_mfma_f32_32x32x16_bf16 v[16:31], v[128:131], v[160:163], v[16:31]
	v_max3_f32 v160, v164, v64, v65
	v_max3_f32 v160, v160, v66, v67
	v_max3_f32 v160, v160, v68, v69
	v_mfma_f32_32x32x16_bf16 v[16:31], v[132:135], v[232:235], v[16:31]
	ds_read_b64_tr_b16 v[232:233], v167 offset:0x200
	ds_read_b64_tr_b16 v[234:235], v167 offset:0xa00
	v_max3_f32 v160, v160, v70, v71
	v_max3_f32 v160, v160, v72, v73
	v_max3_f32 v160, v160, v74, v75
	v_mfma_f32_32x32x16_bf16 v[16:31], v[136:139], v[236:239], v[16:31]
	ds_read_b64_tr_b16 v[236:237], v167 offset:0x1200
	ds_read_b64_tr_b16 v[238:239], v167 offset:0x1a00
	ds_read_b64_tr_b16 v[244:245], v167 offset:0x2200
	ds_read_b64_tr_b16 v[246:247], v167 offset:0x2a00
	ds_read_b64_tr_b16 v[248:249], v167 offset:0x3200
	ds_read_b64_tr_b16 v[250:251], v167 offset:0x3a00
	v_max3_f32 v160, v160, v76, v77
	v_max3_f32 v160, v160, v78, v79
	v_mov_b32_e32 v161, v160
	v_mfma_f32_32x32x16_bf16 v[16:31], v[208:211], v[240:243], v[16:31]
	v_max_f32_e32 v162, v198, v198
	v_permlane32_swap_b32_e32 v160, v161
	v_max_f32_e32 v161, v161, v161
	v_max_f32_e32 v160, v160, v160
	v_max_f32_e32 v160, v160, v161
	s_waitcnt lgkmcnt(0)
	v_mfma_f32_32x32x16_bf16 v[32:47], v[128:131], v[232:235], v[32:47]
	ds_read_b64_tr_b16 v[232:233], v167 offset:0x400
	ds_read_b64_tr_b16 v[234:235], v167 offset:0xc00
	v_sub_f32_e32 v161, v160, v198
	v_max_f32_e32 v160, v162, v160
	v_sub_f32_e32 v162, v198, v160
	v_mul_f32_e32 v162, 0x3dd53b94, v162
	v_exp_f32_e32 v162, v162
	v_mfma_f32_32x32x16_bf16 v[32:47], v[132:135], v[236:239], v[32:47]
	ds_read_b64_tr_b16 v[236:237], v167 offset:0x1400
	ds_read_b64_tr_b16 v[238:239], v167 offset:0x1c00
	ds_read_b64_tr_b16 v[240:241], v167 offset:0x2400
	ds_read_b64_tr_b16 v[242:243], v167 offset:0x2c00
	v_cmp_ge_f32_e32 vcc, s48, v161
	s_cmp_eq_u64 vcc, exec
	s_cselect_b64 s[6:7], -1, 0
	v_cndmask_b32_e64 v206, v162, 1.0, s[6:7]
	v_cndmask_b32_e64 v160, v160, v198, s[6:7]
	v_mul_f32_e32 v205, 0xbdd53b94, v160
	v_cmp_gt_f32_e32 vcc, 1.0, v206
	v_mfma_f32_32x32x16_bf16 v[32:47], v[136:139], v[244:247], v[32:47]
	ds_read_b64_tr_b16 v[244:245], v167 offset:0x3400
	ds_read_b64_tr_b16 v[246:247], v167 offset:0x3c00
	v_fmamk_f32 v87, v87, 0x3dd53b94, v205
	v_fmamk_f32 v80, v80, 0x3dd53b94, v205
	v_fmamk_f32 v81, v81, 0x3dd53b94, v205
	v_fmamk_f32 v82, v82, 0x3dd53b94, v205
	v_fmamk_f32 v83, v83, 0x3dd53b94, v205
	v_mfma_f32_32x32x16_bf16 v[32:47], v[208:211], v[248:251], v[32:47]
	v_fmamk_f32 v84, v84, 0x3dd53b94, v205
	v_fmamk_f32 v85, v85, 0x3dd53b94, v205
	v_fmamk_f32 v86, v86, 0x3dd53b94, v205
	v_fmamk_f32 v88, v88, 0x3dd53b94, v205
	v_fmamk_f32 v89, v89, 0x3dd53b94, v205
	s_waitcnt lgkmcnt(0)
	v_mfma_f32_32x32x16_bf16 v[0:15], v[128:131], v[232:235], v[0:15]
	ds_read_b64_tr_b16 v[232:233], v167 offset:0x600
	ds_read_b64_tr_b16 v[234:235], v167 offset:0xe00
	v_fmamk_f32 v90, v90, 0x3dd53b94, v205
	v_fmamk_f32 v91, v91, 0x3dd53b94, v205
	v_fmamk_f32 v92, v92, 0x3dd53b94, v205
	v_fmamk_f32 v93, v93, 0x3dd53b94, v205
	v_fmamk_f32 v94, v94, 0x3dd53b94, v205
	v_mfma_f32_32x32x16_bf16 v[0:15], v[132:135], v[236:239], v[0:15]
	ds_read_b64_tr_b16 v[236:237], v167 offset:0x1600
	ds_read_b64_tr_b16 v[238:239], v167 offset:0x1e00
	v_fmamk_f32 v95, v95, 0x3dd53b94, v205
	v_fmamk_f32 v215, v64, 0x3dd53b94, v205
	v_fmamk_f32 v216, v65, 0x3dd53b94, v205
	v_fmamk_f32 v217, v66, 0x3dd53b94, v205
	v_fmamk_f32 v218, v67, 0x3dd53b94, v205
	v_mfma_f32_32x32x16_bf16 v[0:15], v[136:139], v[240:243], v[0:15]
	ds_read_b64_tr_b16 v[240:241], v167 offset:0x2600
	ds_read_b64_tr_b16 v[242:243], v167 offset:0x2e00
	ds_read_b64_tr_b16 v[248:249], v167 offset:0x3600
	ds_read_b64_tr_b16 v[250:251], v167 offset:0x3e00
	v_fmamk_f32 v219, v68, 0x3dd53b94, v205
	v_fmamk_f32 v212, v73, 0x3dd53b94, v205
	v_fmamk_f32 v213, v74, 0x3dd53b94, v205
	v_fmamk_f32 v214, v75, 0x3dd53b94, v205
	v_mfma_f32_32x32x16_bf16 v[0:15], v[208:211], v[244:247], v[0:15]
	v_fmamk_f32 v207, v76, 0x3dd53b94, v205
	v_fmamk_f32 v220, v77, 0x3dd53b94, v205
	v_fmamk_f32 v221, v78, 0x3dd53b94, v205
	s_waitcnt lgkmcnt(0)
	v_mfma_f32_32x32x16_bf16 v[48:63], v[128:131], v[232:235], v[48:63]
	v_exp_f32_e32 v128, v80
	v_exp_f32_e32 v129, v82
	v_exp_f32_e32 v130, v84
	v_exp_f32_e32 v131, v86
	v_mfma_f32_32x32x16_bf16 v[48:63], v[132:135], v[236:239], v[48:63]
	v_exp_f32_e32 v132, v88
	v_exp_f32_e32 v133, v90
	v_exp_f32_e32 v134, v92
	v_exp_f32_e32 v135, v94
	v_mfma_f32_32x32x16_bf16 v[48:63], v[136:139], v[240:243], v[48:63]
	v_exp_f32_e32 v139, v89
	v_exp_f32_e32 v138, v91
	v_exp_f32_e32 v137, v93
	v_exp_f32_e32 v136, v95
	v_mfma_f32_32x32x16_bf16 v[48:63], v[208:211], v[248:251], v[48:63]
	v_exp_f32_e32 v161, v87
	v_exp_f32_e32 v198, v81
	v_exp_f32_e32 v163, v83
	v_exp_f32_e32 v162, v85
	v_fmamk_f32 v208, v69, 0x3dd53b94, v205
	v_fmamk_f32 v209, v70, 0x3dd53b94, v205
	v_fmamk_f32 v210, v71, 0x3dd53b94, v205
	v_fmamk_f32 v211, v72, 0x3dd53b94, v205
	v_fmac_f32_e32 v205, 0x3dd53b94, v79
	s_cbranch_vccz .LBB0_761
	s_and_saveexec_b64 s[8:9], s[4:5]
	ds_write_b32 v189, v206 offset:128
	s_or_b64 exec, exec, s[8:9]
	s_waitcnt lgkmcnt(0)
	v_add_u32_e32 v248, s62, v169
	ds_read_b128 v[232:235], v248 offset:224
	ds_read_b128 v[236:239], v248 offset:192
	ds_read_b128 v[240:243], v248 offset:160
	ds_read_b128 v[244:247], v248 offset:128
	s_waitcnt lgkmcnt(3)
	v_pk_mul_f32 v[28:29], v[28:29], v[232:233]
	s_waitcnt lgkmcnt(2)
	v_pk_mul_f32 v[24:25], v[24:25], v[236:237]
	s_waitcnt lgkmcnt(1)
	v_pk_mul_f32 v[20:21], v[20:21], v[240:241]
	v_pk_mul_f32 v[30:31], v[30:31], v[234:235]
	v_pk_mul_f32 v[26:27], v[26:27], v[238:239]
	v_pk_mul_f32 v[22:23], v[22:23], v[242:243]
	s_waitcnt lgkmcnt(0)
	v_pk_mul_f32 v[18:19], v[18:19], v[246:247]
	v_pk_mul_f32 v[16:17], v[16:17], v[244:245]
	v_pk_mul_f32 v[44:45], v[44:45], v[232:233]
	v_pk_mul_f32 v[40:41], v[40:41], v[236:237]
	v_pk_mul_f32 v[36:37], v[36:37], v[240:241]
	v_pk_mul_f32 v[46:47], v[46:47], v[234:235]
	v_pk_mul_f32 v[42:43], v[42:43], v[238:239]
	v_pk_mul_f32 v[38:39], v[38:39], v[242:243]
	v_pk_mul_f32 v[34:35], v[34:35], v[246:247]
	v_pk_mul_f32 v[32:33], v[32:33], v[244:245]
	v_pk_mul_f32 v[12:13], v[12:13], v[232:233]
	v_pk_mul_f32 v[8:9], v[8:9], v[236:237]
	v_pk_mul_f32 v[4:5], v[4:5], v[240:241]
	v_pk_mul_f32 v[14:15], v[14:15], v[234:235]
	v_pk_mul_f32 v[10:11], v[10:11], v[238:239]
	v_pk_mul_f32 v[6:7], v[6:7], v[242:243]
	v_pk_mul_f32 v[2:3], v[2:3], v[246:247]
	v_pk_mul_f32 v[0:1], v[0:1], v[244:245]
	v_pk_mul_f32 v[60:61], v[60:61], v[232:233]
	v_pk_mul_f32 v[56:57], v[56:57], v[236:237]
	v_pk_mul_f32 v[52:53], v[52:53], v[240:241]
	v_pk_mul_f32 v[62:63], v[62:63], v[234:235]
	v_pk_mul_f32 v[58:59], v[58:59], v[238:239]
	v_pk_mul_f32 v[54:55], v[54:55], v[242:243]
	v_pk_mul_f32 v[50:51], v[50:51], v[246:247]
	v_pk_mul_f32 v[48:49], v[48:49], v[244:245]
.LBB0_761:
	s_waitcnt vmcnt(0) lgkmcnt(0)
	s_barrier
	s_add_i32 s80, s10, 64
	s_cmp_lt_u32 s12, 2
	s_cselect_b32 s80, s80, s11
	s_mul_i32 s81, s80, 0xc00
	s_add_i32 s85, s82, 0xc000
	s_mov_b32 m0, s85
	s_add_i32 s85, s82, 0x12000
	buffer_load_dwordx4 v154, s[72:75], s81 offen lds
	s_mov_b32 m0, s85
	s_add_i32 s85, s82, 0xe000
	buffer_load_dwordx4 v155, s[72:75], s81 offen lds
	s_mov_b32 m0, s85
	s_add_i32 s81, s81, 0x18000
	buffer_load_dwordx4 v154, s[72:75], s81 offen lds
	s_lshl_b32 s81, s84, 11
	s_add_i32 s85, s82, 0x0
	s_mov_b32 m0, s85
	s_add_i32 s85, s82, 0x2000
	buffer_load_dwordx4 v196, s[76:79], s81 offen lds
	s_mov_b32 m0, s85
	s_add_i32 s81, s81, 0x10000
	buffer_load_dwordx4 v196, s[76:79], s81 offen lds
	s_mov_b32 s83, s80
	ds_read_b128 v[64:67], v180 offset:32768
	ds_read_b128 v[68:71], v180 offset:40960
	ds_read_b128 v[222:225], v181 offset:32768
	ds_read_b128 v[226:229], v181 offset:40960
	ds_read_b128 v[230:233], v182 offset:32768
	ds_read_b128 v[234:237], v182 offset:40960
	ds_read_b128 v[238:241], v183 offset:32768
	ds_read_b128 v[242:245], v183 offset:40960
	v_exp_f32_e32 v164, v215
	v_add_f32_e32 v215, 0, v128
	s_waitcnt lgkmcnt(7)
	v_mfma_f32_32x32x16_bf16 v[80:95], v[64:67], v[124:127], 0
	v_add_f32_e32 v215, v198, v215
	v_add_f32_e32 v215, v129, v215
	v_add_f32_e32 v215, v163, v215
	v_add_f32_e32 v215, v130, v215
	v_add_f32_e32 v215, v162, v215
	v_add_f32_e32 v215, v131, v215
	v_add_f32_e32 v215, v161, v215
	s_waitcnt lgkmcnt(6)
	v_mfma_f32_32x32x16_bf16 v[64:79], v[68:71], v[124:127], 0
	v_add_f32_e32 v215, v132, v215
	v_add_f32_e32 v215, v139, v215
	v_add_f32_e32 v215, v133, v215
	v_add_f32_e32 v215, v138, v215
	v_add_f32_e32 v215, v134, v215
	v_exp_f32_e32 v165, v216
	v_add_f32_e32 v215, v137, v215
	s_waitcnt lgkmcnt(5)
	v_mfma_f32_32x32x16_bf16 v[80:95], v[222:225], v[120:123], v[80:95]
	v_exp_f32_e32 v217, v217
	v_add_f32_e32 v215, v135, v215
	v_exp_f32_e32 v218, v218
	v_add_f32_e32 v215, v136, v215
	v_exp_f32_e32 v219, v219
	v_add_f32_e32 v215, v164, v215
	v_exp_f32_e32 v208, v208
	s_waitcnt lgkmcnt(4)
	v_mfma_f32_32x32x16_bf16 v[64:79], v[226:229], v[120:123], v[64:79]
	ds_read_b128 v[222:225], v184 offset:32768
	ds_read_b128 v[226:229], v184 offset:40960
	v_add_f32_e32 v215, v165, v215
	v_exp_f32_e32 v209, v209
	v_add_f32_e32 v215, v217, v215
	v_exp_f32_e32 v210, v210
	v_add_f32_e32 v215, v218, v215
	v_exp_f32_e32 v211, v211
	s_waitcnt lgkmcnt(5)
	v_mfma_f32_32x32x16_bf16 v[80:95], v[230:233], v[116:119], v[80:95]
	v_add_f32_e32 v215, v219, v215
	v_exp_f32_e32 v212, v212
	v_add_f32_e32 v215, v208, v215
	v_exp_f32_e32 v213, v213
	v_add_f32_e32 v215, v209, v215
	v_exp_f32_e32 v214, v214
	v_add_f32_e32 v215, v210, v215
	s_waitcnt lgkmcnt(4)
	v_mfma_f32_32x32x16_bf16 v[64:79], v[234:237], v[116:119], v[64:79]
	ds_read_b128 v[230:233], v185 offset:32768
	ds_read_b128 v[234:237], v185 offset:40960
	v_exp_f32_e32 v207, v207
	v_add_f32_e32 v215, v211, v215
	v_exp_f32_e32 v220, v220
	v_add_f32_e32 v215, v212, v215
	v_exp_f32_e32 v221, v221
	v_add_f32_e32 v215, v213, v215
	s_waitcnt lgkmcnt(5)
	v_mfma_f32_32x32x16_bf16 v[80:95], v[238:241], v[112:115], v[80:95]
	v_exp_f32_e32 v205, v205
	v_add_f32_e32 v215, v214, v215
	v_add_f32_e32 v215, v207, v215
	v_add_f32_e32 v215, v220, v215
	v_add_f32_e32 v215, v221, v215
	v_add_f32_e32 v215, v205, v215
	v_mov_b32_e32 v216, v215
	s_waitcnt lgkmcnt(4)
	v_mfma_f32_32x32x16_bf16 v[64:79], v[242:245], v[112:115], v[64:79]
	ds_read_b128 v[238:241], v186 offset:32768
	ds_read_b128 v[242:245], v186 offset:40960
	v_permlane32_swap_b32_e32 v215, v216
	v_cvt_pk_bf16_f32 v128, v128, v198
	v_cvt_pk_bf16_f32 v129, v129, v163
	v_cvt_pk_bf16_f32 v130, v130, v162
	v_cvt_pk_bf16_f32 v131, v131, v161
	s_waitcnt lgkmcnt(5)
	v_mfma_f32_32x32x16_bf16 v[80:95], v[222:225], v[108:111], v[80:95]
	v_cvt_pk_bf16_f32 v132, v132, v139
	v_cvt_pk_bf16_f32 v133, v133, v138
	v_cvt_pk_bf16_f32 v134, v134, v137
	v_cvt_pk_bf16_f32 v135, v135, v136
	v_cvt_pk_bf16_f32 v136, v164, v165
	v_cvt_pk_bf16_f32 v137, v217, v218
	v_cvt_pk_bf16_f32 v138, v219, v208
	s_waitcnt lgkmcnt(4)
	v_mfma_f32_32x32x16_bf16 v[64:79], v[226:229], v[108:111], v[64:79]
	ds_read_b128 v[222:225], v187 offset:32768
	ds_read_b128 v[226:229], v187 offset:40960
	v_cvt_pk_bf16_f32 v139, v209, v210
	v_cvt_pk_bf16_f32 v208, v211, v212
	v_cvt_pk_bf16_f32 v209, v213, v214
	v_cvt_pk_bf16_f32 v210, v207, v220
	v_cvt_pk_bf16_f32 v211, v221, v205
	v_permlane32_swap_b32_e32 v128, v130
	s_waitcnt lgkmcnt(5)
	v_mfma_f32_32x32x16_bf16 v[80:95], v[230:233], v[104:107], v[80:95]
	v_permlane32_swap_b32_e32 v129, v131
	v_permlane32_swap_b32_e32 v132, v134
	v_permlane32_swap_b32_e32 v133, v135
	v_permlane32_swap_b32_e32 v136, v138
	s_waitcnt lgkmcnt(4)
	v_mfma_f32_32x32x16_bf16 v[64:79], v[234:237], v[104:107], v[64:79]
	ds_read_b128 v[230:233], v191
	ds_read_b128 v[234:237], v191 offset:4096
	v_permlane32_swap_b32_e32 v137, v139
	v_permlane32_swap_b32_e32 v208, v210
	v_permlane32_swap_b32_e32 v209, v211
	s_waitcnt lgkmcnt(5)
	v_mfma_f32_32x32x16_bf16 v[80:95], v[238:241], v[100:103], v[80:95]
	s_waitcnt lgkmcnt(4)
	v_mfma_f32_32x32x16_bf16 v[64:79], v[242:245], v[100:103], v[64:79]
	ds_read_b128 v[238:241], v192
	ds_read_b128 v[242:245], v192 offset:4096
	s_waitcnt lgkmcnt(5)
	v_mfma_f32_32x32x16_bf16 v[80:95], v[222:225], v[96:99], v[80:95]
	s_waitcnt lgkmcnt(4)
	v_mfma_f32_32x32x16_bf16 v[64:79], v[226:229], v[96:99], v[64:79]
	ds_read_b128 v[222:225], v193
	ds_read_b128 v[226:229], v193 offset:4096
	s_waitcnt lgkmcnt(5)
	v_mfma_f32_32x32x16_bf16 v[80:95], v[230:233], v[142:145], v[80:95]
	s_waitcnt lgkmcnt(4)
	v_mfma_f32_32x32x16_bf16 v[64:79], v[234:237], v[142:145], v[64:79]
	ds_read_b128 v[230:233], v194
	ds_read_b128 v[234:237], v194 offset:4096
	s_waitcnt lgkmcnt(5)
	v_mfma_f32_32x32x16_bf16 v[80:95], v[238:241], v[146:149], v[80:95]
	s_waitcnt lgkmcnt(4)
	v_mfma_f32_32x32x16_bf16 v[64:79], v[242:245], v[146:149], v[64:79]
	s_waitcnt lgkmcnt(3)
	v_mfma_f32_32x32x16_bf16 v[80:95], v[222:225], v[150:153], v[80:95]
	s_waitcnt lgkmcnt(2)
	v_mfma_f32_32x32x16_bf16 v[64:79], v[226:229], v[150:153], v[64:79]
	s_waitcnt lgkmcnt(1)
	v_mfma_f32_32x32x16_bf16 v[80:95], v[230:233], v[156:159], v[80:95]
	s_waitcnt lgkmcnt(0)
	v_mfma_f32_32x32x16_bf16 v[64:79], v[234:237], v[156:159], v[64:79]
	ds_read_b64_tr_b16 v[238:239], v174 offset:0
	ds_read_b64_tr_b16 v[240:241], v174 offset:0x800
	ds_read_b64_tr_b16 v[242:243], v174 offset:0x1000
	ds_read_b64_tr_b16 v[244:245], v174 offset:0x1800
	ds_read_b64_tr_b16 v[246:247], v174 offset:0x2000
	ds_read_b64_tr_b16 v[248:249], v174 offset:0x2800
	ds_read_b64_tr_b16 v[250:251], v174 offset:0x3000
	ds_read_b64_tr_b16 v[252:253], v174 offset:0x3800
	s_nop 3
	v_max_f32_e32 v161, v81, v81
	v_max_f32_e32 v162, v80, v80
	v_max_f32_e32 v161, v162, v161
	v_max3_f32 v161, v161, v82, v83
	v_max3_f32 v161, v161, v84, v85
	v_max3_f32 v161, v161, v86, v87
	v_max3_f32 v161, v161, v88, v89
	v_max3_f32 v161, v161, v90, v91
	v_max3_f32 v161, v161, v92, v93
	v_max3_f32 v161, v161, v94, v95
	s_waitcnt lgkmcnt(0)
	v_mfma_f32_32x32x16_bf16 v[16:31], v[128:131], v[238:241], v[16:31]
	ds_read_b64_tr_b16 v[238:239], v174 offset:0x200
	ds_read_b64_tr_b16 v[240:241], v174 offset:0xa00
	v_max3_f32 v161, v161, v64, v65
	v_max3_f32 v161, v161, v66, v67
	v_max3_f32 v161, v161, v68, v69
	v_mfma_f32_32x32x16_bf16 v[16:31], v[132:135], v[242:245], v[16:31]
	ds_read_b64_tr_b16 v[242:243], v174 offset:0x1200
	ds_read_b64_tr_b16 v[244:245], v174 offset:0x1a00
	v_max3_f32 v161, v161, v70, v71
	v_max3_f32 v161, v161, v72, v73
	v_max3_f32 v161, v161, v74, v75
	v_mfma_f32_32x32x16_bf16 v[16:31], v[136:139], v[246:249], v[16:31]
	ds_read_b64_tr_b16 v[246:247], v174 offset:0x2200
	ds_read_b64_tr_b16 v[248:249], v174 offset:0x2a00
	ds_read_b64_tr_b16 v[162:163], v174 offset:0x3200
	ds_read_b64_tr_b16 v[164:165], v174 offset:0x3a00
	v_max3_f32 v161, v161, v76, v77
	v_max3_f32 v161, v161, v78, v79
	v_mov_b32_e32 v198, v161
	v_mfma_f32_32x32x16_bf16 v[16:31], v[208:211], v[250:253], v[16:31]
	v_max_f32_e32 v205, v160, v160
	v_permlane32_swap_b32_e32 v161, v198
	v_max_f32_e32 v198, v198, v198
	v_max_f32_e32 v161, v161, v161
	v_max_f32_e32 v161, v161, v198
	s_waitcnt lgkmcnt(0)
	v_mfma_f32_32x32x16_bf16 v[32:47], v[128:131], v[238:241], v[32:47]
	ds_read_b64_tr_b16 v[238:239], v174 offset:0x400
	ds_read_b64_tr_b16 v[240:241], v174 offset:0xc00
	v_sub_f32_e32 v198, v161, v160
	v_max_f32_e32 v161, v205, v161
	v_sub_f32_e32 v205, v160, v161
	v_mul_f32_e32 v205, 0x3dd53b94, v205
	v_exp_f32_e32 v205, v205
	v_mfma_f32_32x32x16_bf16 v[32:47], v[132:135], v[242:245], v[32:47]
	ds_read_b64_tr_b16 v[242:243], v174 offset:0x1400
	ds_read_b64_tr_b16 v[244:245], v174 offset:0x1c00
	v_cmp_ge_f32_e32 vcc, s48, v198
	s_cmp_eq_u64 vcc, exec
	s_cselect_b64 s[6:7], -1, 0
	v_cndmask_b32_e64 v205, v205, 1.0, s[6:7]
	v_cndmask_b32_e64 v198, v161, v160, s[6:7]
	v_mul_f32_e32 v236, 0xbdd53b94, v198
	v_mov_b32_e32 v237, v236
	v_cmp_gt_f32_e32 vcc, 1.0, v205
	v_mfma_f32_32x32x16_bf16 v[32:47], v[136:139], v[246:249], v[32:47]
	ds_read_b64_tr_b16 v[246:247], v174 offset:0x2400
	ds_read_b64_tr_b16 v[248:249], v174 offset:0x2c00
	ds_read_b64_tr_b16 v[250:251], v174 offset:0x3400
	ds_read_b64_tr_b16 v[252:253], v174 offset:0x3c00
	v_fmamk_f32 v80, v80, 0x3dd53b94, v236
	v_fmamk_f32 v81, v81, 0x3dd53b94, v236
	v_fmamk_f32 v82, v82, 0x3dd53b94, v236
	v_fmamk_f32 v83, v83, 0x3dd53b94, v236
	v_mfma_f32_32x32x16_bf16 v[32:47], v[208:211], v[162:165], v[32:47]
	v_fmamk_f32 v84, v84, 0x3dd53b94, v236
	v_fmamk_f32 v85, v85, 0x3dd53b94, v236
	v_fmamk_f32 v86, v86, 0x3dd53b94, v236
	v_fmamk_f32 v87, v87, 0x3dd53b94, v236
	s_waitcnt lgkmcnt(0)
	v_mfma_f32_32x32x16_bf16 v[0:15], v[128:131], v[238:241], v[0:15]
	ds_read_b64_tr_b16 v[162:163], v174 offset:0x600
	ds_read_b64_tr_b16 v[164:165], v174 offset:0xe00
	ds_read_b64_tr_b16 v[238:239], v174 offset:0x1600
	ds_read_b64_tr_b16 v[240:241], v174 offset:0x1e00
	v_fmamk_f32 v88, v88, 0x3dd53b94, v236
	v_fmamk_f32 v89, v89, 0x3dd53b94, v236
	v_fmamk_f32 v90, v90, 0x3dd53b94, v236
	v_fmamk_f32 v91, v91, 0x3dd53b94, v236
	v_mfma_f32_32x32x16_bf16 v[0:15], v[132:135], v[242:245], v[0:15]
	ds_read_b64_tr_b16 v[242:243], v174 offset:0x2600
	ds_read_b64_tr_b16 v[244:245], v174 offset:0x2e00
	v_fmamk_f32 v92, v92, 0x3dd53b94, v236
	v_fmamk_f32 v93, v93, 0x3dd53b94, v236
	v_fmamk_f32 v94, v94, 0x3dd53b94, v236
	v_fmamk_f32 v95, v95, 0x3dd53b94, v236
	v_mfma_f32_32x32x16_bf16 v[0:15], v[136:139], v[246:249], v[0:15]
	ds_read_b64_tr_b16 v[246:247], v174 offset:0x3600
	ds_read_b64_tr_b16 v[248:249], v174 offset:0x3e00
	v_exp_f32_e32 v222, v80
	v_exp_f32_e32 v224, v81
	v_exp_f32_e32 v220, v82
	v_mfma_f32_32x32x16_bf16 v[0:15], v[208:211], v[250:253], v[0:15]
	v_exp_f32_e32 v223, v83
	v_exp_f32_e32 v219, v84
	v_exp_f32_e32 v221, v85
	s_waitcnt lgkmcnt(0)
	v_mfma_f32_32x32x16_bf16 v[48:63], v[128:131], v[162:165], v[48:63]
	v_exp_f32_e32 v217, v86
	v_exp_f32_e32 v218, v87
	v_exp_f32_e32 v212, v88
	v_pk_fma_f32 v[130:131], v[70:71], s[28:29], v[236:237] op_sel_hi:[1,0,0]
	v_pk_fma_f32 v[128:129], v[72:73], s[28:29], v[236:237] op_sel_hi:[1,0,0]
	v_mfma_f32_32x32x16_bf16 v[48:63], v[132:135], v[238:241], v[48:63]
	v_exp_f32_e32 v214, v89
	v_exp_f32_e32 v213, v91
	v_exp_f32_e32 v207, v94
	v_pk_fma_f32 v[132:133], v[68:69], s[28:29], v[236:237] op_sel_hi:[1,0,0]
	v_pk_fma_f32 v[134:135], v[78:79], s[28:29], v[236:237] op_sel_hi:[1,0,0]
	v_mfma_f32_32x32x16_bf16 v[48:63], v[136:139], v[242:245], v[48:63]
	v_pk_fma_f32 v[138:139], v[64:65], s[28:29], v[236:237] op_sel_hi:[1,0,0]
	v_pk_fma_f32 v[136:137], v[66:67], s[28:29], v[236:237] op_sel_hi:[1,0,0]
	v_pk_fma_f32 v[162:163], v[74:75], s[28:29], v[236:237] op_sel_hi:[1,0,0]
	v_pk_fma_f32 v[160:161], v[76:77], s[28:29], v[236:237] op_sel_hi:[1,0,0]
	v_mfma_f32_32x32x16_bf16 v[48:63], v[208:211], v[246:249], v[48:63]
	v_exp_f32_e32 v211, v90
	v_exp_f32_e32 v208, v92
	v_exp_f32_e32 v210, v93
	v_exp_f32_e32 v209, v95
	v_add_f32_e32 v64, v203, v204
	v_fmac_f32_e32 v64, v197, v140
	v_add_f32_e32 v140, v215, v216
	s_addk_i32 s10, 0x80
	s_add_i32 s64, s64, 2
	s_addk_i32 s11, 0x80
	v_fmac_f32_e32 v140, v64, v206
	s_cbranch_vccz .LBB0_765
	s_and_saveexec_b64 s[8:9], s[4:5]
	ds_write_b32 v189, v205 offset:128
	s_or_b64 exec, exec, s[8:9]
	s_waitcnt lgkmcnt(0)
	v_add_u32_e32 v164, s62, v169
	ds_read_b128 v[238:241], v164 offset:224
	ds_read_b128 v[242:245], v164 offset:192
	ds_read_b128 v[246:249], v164 offset:160
	ds_read_b128 v[250:253], v164 offset:128
	s_waitcnt lgkmcnt(3)
	v_pk_mul_f32 v[28:29], v[28:29], v[238:239]
	s_waitcnt lgkmcnt(2)
	v_pk_mul_f32 v[24:25], v[24:25], v[242:243]
	s_waitcnt lgkmcnt(1)
	v_pk_mul_f32 v[20:21], v[20:21], v[246:247]
	v_pk_mul_f32 v[30:31], v[30:31], v[240:241]
	v_pk_mul_f32 v[26:27], v[26:27], v[244:245]
	v_pk_mul_f32 v[22:23], v[22:23], v[248:249]
	s_waitcnt lgkmcnt(0)
	v_pk_mul_f32 v[18:19], v[18:19], v[252:253]
	v_pk_mul_f32 v[16:17], v[16:17], v[250:251]
	v_pk_mul_f32 v[44:45], v[44:45], v[238:239]
	v_pk_mul_f32 v[40:41], v[40:41], v[242:243]
	v_pk_mul_f32 v[36:37], v[36:37], v[246:247]
	v_pk_mul_f32 v[46:47], v[46:47], v[240:241]
	v_pk_mul_f32 v[42:43], v[42:43], v[244:245]
	v_pk_mul_f32 v[38:39], v[38:39], v[248:249]
	v_pk_mul_f32 v[34:35], v[34:35], v[252:253]
	v_pk_mul_f32 v[32:33], v[32:33], v[250:251]
	v_pk_mul_f32 v[12:13], v[12:13], v[238:239]
	v_pk_mul_f32 v[8:9], v[8:9], v[242:243]
	v_pk_mul_f32 v[4:5], v[4:5], v[246:247]
	v_pk_mul_f32 v[14:15], v[14:15], v[240:241]
	v_pk_mul_f32 v[10:11], v[10:11], v[244:245]
	v_pk_mul_f32 v[6:7], v[6:7], v[248:249]
	v_pk_mul_f32 v[2:3], v[2:3], v[252:253]
	v_pk_mul_f32 v[0:1], v[0:1], v[250:251]
	v_pk_mul_f32 v[60:61], v[60:61], v[238:239]
	v_pk_mul_f32 v[56:57], v[56:57], v[242:243]
	v_pk_mul_f32 v[52:53], v[52:53], v[246:247]
	v_pk_mul_f32 v[62:63], v[62:63], v[240:241]
	v_pk_mul_f32 v[58:59], v[58:59], v[244:245]
	v_pk_mul_f32 v[54:55], v[54:55], v[248:249]
	v_pk_mul_f32 v[50:51], v[50:51], v[252:253]
	v_pk_mul_f32 v[48:49], v[48:49], v[250:251]

.LBB0_767:
	s_lshl_b32 s81, s83, 11
	s_add_i32 s85, s82, 0x4000
	s_mov_b32 m0, s85
	s_add_i32 s85, s82, 0x6000
	buffer_load_dwordx4 v196, s[76:79], s81 offen lds
	s_mov_b32 m0, s85
	s_add_i32 s81, s81, 0x10000
	buffer_load_dwordx4 v196, s[76:79], s81 offen lds
	ds_read_b128 v[64:67], v180 offset:49152
	ds_read_b128 v[68:71], v180 offset:57344
	v_exp_f32_e32 v138, v138
	v_exp_f32_e32 v139, v139
	v_exp_f32_e32 v136, v136
	s_waitcnt lgkmcnt(1)
	v_mfma_f32_32x32x16_bf16 v[80:95], v[64:67], v[124:127], 0
	v_exp_f32_e32 v137, v137
	v_exp_f32_e32 v132, v132
	v_exp_f32_e32 v128, v128
	v_exp_f32_e32 v129, v129
	s_waitcnt lgkmcnt(0)
	v_mfma_f32_32x32x16_bf16 v[64:79], v[68:71], v[124:127], 0
	ds_read_b128 v[124:127], v181 offset:49152
	ds_read_b128 v[154:157], v181 offset:57344
	s_waitcnt lgkmcnt(1)
	v_mfma_f32_32x32x16_bf16 v[80:95], v[124:127], v[120:123], v[80:95]
	s_waitcnt lgkmcnt(0)
	v_mfma_f32_32x32x16_bf16 v[64:79], v[154:157], v[120:123], v[64:79]
	ds_read_b128 v[120:123], v182 offset:49152
	ds_read_b128 v[124:127], v182 offset:57344
	s_waitcnt lgkmcnt(1)
	v_mfma_f32_32x32x16_bf16 v[80:95], v[120:123], v[116:119], v[80:95]
	s_waitcnt lgkmcnt(0)
	v_mfma_f32_32x32x16_bf16 v[64:79], v[124:127], v[116:119], v[64:79]
	ds_read_b128 v[116:119], v183 offset:49152
	ds_read_b128 v[120:123], v183 offset:57344
	s_waitcnt lgkmcnt(1)
	v_mfma_f32_32x32x16_bf16 v[80:95], v[116:119], v[112:115], v[80:95]
	s_waitcnt lgkmcnt(0)
	v_mfma_f32_32x32x16_bf16 v[64:79], v[120:123], v[112:115], v[64:79]
	ds_read_b128 v[112:115], v184 offset:49152
	ds_read_b128 v[116:119], v184 offset:57344
	s_waitcnt lgkmcnt(1)
	v_mfma_f32_32x32x16_bf16 v[80:95], v[112:115], v[108:111], v[80:95]
	ds_read_b128 v[112:115], v185 offset:49152
	s_waitcnt lgkmcnt(1)
	v_mfma_f32_32x32x16_bf16 v[64:79], v[116:119], v[108:111], v[64:79]
	ds_read_b128 v[108:111], v185 offset:57344
	ds_read_b128 v[116:119], v186 offset:49152
	ds_read_b128 v[120:123], v186 offset:57344
	ds_read_b128 v[124:127], v187 offset:49152
	ds_read_b128 v[154:157], v187 offset:57344
	ds_read_b128 v[192:195], v199
	ds_read_b128 v[226:229], v199 offset:4096
	s_waitcnt lgkmcnt(7)
	v_mfma_f32_32x32x16_bf16 v[80:95], v[112:115], v[104:107], v[80:95]
	ds_read_b128 v[112:115], v200
	ds_read_b128 v[230:233], v200 offset:4096
	ds_read_b128 v[234:237], v190
	ds_read_b128 v[238:241], v190 offset:1024
	ds_read_b128 v[242:245], v201
	ds_read_b128 v[246:249], v201 offset:4096
	ds_read_b128 v[250:253], v202
	ds_read_b128 v[200:203], v202 offset:4096
	s_waitcnt lgkmcnt(14)
	v_mfma_f32_32x32x16_bf16 v[64:79], v[108:111], v[104:107], v[64:79]
	ds_read_b128 v[104:107], v190 offset:2048
	ds_read_b128 v[108:111], v190 offset:3072
	s_waitcnt lgkmcnt(14)
	v_mfma_f32_32x32x16_bf16 v[80:95], v[116:119], v[100:103], v[80:95]
	v_exp_f32_e32 v118, v133
	v_exp_f32_e32 v119, v130
	v_exp_f32_e32 v130, v131
	v_exp_f32_e32 v131, v162
	v_exp_f32_e32 v133, v163
	v_cvt_pk_bf16_f32 v116, v138, v139
	v_cvt_pk_bf16_f32 v117, v136, v137
	v_mfma_f32_32x32x16_bf16 v[64:79], v[120:123], v[100:103], v[64:79]
	v_add_f32_e32 v100, 0, v222
	v_add_f32_e32 v100, v224, v100
	v_add_f32_e32 v100, v220, v100
	v_add_f32_e32 v100, v223, v100
	v_add_f32_e32 v100, v219, v100
	v_add_f32_e32 v100, v221, v100
	v_add_f32_e32 v100, v217, v100
	s_waitcnt lgkmcnt(13)
	v_mfma_f32_32x32x16_bf16 v[80:95], v[124:127], v[96:99], v[80:95]
	v_add_f32_e32 v100, v218, v100
	v_add_f32_e32 v100, v212, v100
	v_add_f32_e32 v100, v214, v100
	v_exp_f32_e32 v120, v160
	v_exp_f32_e32 v121, v161
	v_exp_f32_e32 v122, v134
	v_exp_f32_e32 v123, v135
	s_waitcnt lgkmcnt(12)
	v_mfma_f32_32x32x16_bf16 v[64:79], v[154:157], v[96:99], v[64:79]
	v_add_f32_e32 v96, v211, v100
	v_add_f32_e32 v96, v213, v96
	v_add_f32_e32 v96, v208, v96
	v_add_f32_e32 v96, v210, v96
	v_add_f32_e32 v96, v207, v96
	v_add_f32_e32 v96, v209, v96
	v_add_f32_e32 v96, v138, v96
	s_waitcnt lgkmcnt(7)
	v_mfma_f32_32x32x16_bf16 v[80:95], v[192:195], v[234:237], v[80:95]
	v_add_f32_e32 v96, v139, v96
	v_add_f32_e32 v96, v136, v96
	v_add_f32_e32 v96, v137, v96
	v_add_f32_e32 v96, v132, v96
	v_add_f32_e32 v96, v118, v96
	v_add_f32_e32 v96, v119, v96
	v_add_f32_e32 v96, v130, v96
	v_mfma_f32_32x32x16_bf16 v[64:79], v[226:229], v[234:237], v[64:79]
	v_add_f32_e32 v96, v128, v96
	v_add_f32_e32 v96, v129, v96
	v_add_f32_e32 v96, v131, v96
	v_add_f32_e32 v96, v133, v96
	v_add_f32_e32 v96, v120, v96
	v_add_f32_e32 v96, v121, v96
	v_add_f32_e32 v96, v122, v96
	s_waitcnt lgkmcnt(6)
	v_mfma_f32_32x32x16_bf16 v[80:95], v[112:115], v[238:241], v[80:95]
	v_add_f32_e32 v96, v123, v96
	v_mov_b32_e32 v97, v96
	s_nop 1
	v_permlane32_swap_b32_e32 v96, v97
	v_cvt_pk_bf16_f32 v100, v222, v224
	v_cvt_pk_bf16_f32 v101, v220, v223
	v_cvt_pk_bf16_f32 v102, v219, v221
	v_mfma_f32_32x32x16_bf16 v[64:79], v[230:233], v[238:241], v[64:79]
	v_cvt_pk_bf16_f32 v103, v217, v218
	v_cvt_pk_bf16_f32 v112, v212, v214
	v_cvt_pk_bf16_f32 v113, v211, v213
	v_cvt_pk_bf16_f32 v114, v208, v210
	v_cvt_pk_bf16_f32 v115, v207, v209
	v_cvt_pk_bf16_f32 v118, v132, v118
	v_cvt_pk_bf16_f32 v119, v119, v130
	s_waitcnt lgkmcnt(1)
	v_mfma_f32_32x32x16_bf16 v[80:95], v[242:245], v[104:107], v[80:95]
	v_permlane32_swap_b32_e32 v100, v102
	v_permlane32_swap_b32_e32 v101, v103
	v_permlane32_swap_b32_e32 v112, v114
	v_permlane32_swap_b32_e32 v113, v115
	v_mfma_f32_32x32x16_bf16 v[64:79], v[246:249], v[104:107], v[64:79]
	v_cvt_pk_bf16_f32 v104, v128, v129
	v_cvt_pk_bf16_f32 v105, v131, v133
	v_cvt_pk_bf16_f32 v106, v120, v121
	v_cvt_pk_bf16_f32 v107, v122, v123
	v_permlane32_swap_b32_e32 v116, v118
	v_permlane32_swap_b32_e32 v117, v119
	s_waitcnt lgkmcnt(0)
	v_mfma_f32_32x32x16_bf16 v[80:95], v[250:253], v[108:111], v[80:95]
	v_permlane32_swap_b32_e32 v104, v106
	v_permlane32_swap_b32_e32 v105, v107
	v_mfma_f32_32x32x16_bf16 v[64:79], v[200:203], v[108:111], v[64:79]
	ds_read_b64_tr_b16 v[108:109], v167 offset:0
	ds_read_b64_tr_b16 v[110:111], v167 offset:0x800
	ds_read_b64_tr_b16 v[120:121], v167 offset:0x1000
	ds_read_b64_tr_b16 v[122:123], v167 offset:0x1800
	ds_read_b64_tr_b16 v[124:125], v167 offset:0x2000
	ds_read_b64_tr_b16 v[126:127], v167 offset:0x2800
	ds_read_b64_tr_b16 v[128:129], v167 offset:0x3000
	ds_read_b64_tr_b16 v[130:131], v167 offset:0x3800
	s_nop 8
	v_max_f32_e32 v98, v81, v81
	v_max_f32_e32 v99, v80, v80
	v_max_f32_e32 v98, v99, v98
	v_max3_f32 v98, v98, v82, v83
	v_max3_f32 v98, v98, v84, v85
	v_max3_f32 v98, v98, v86, v87
	v_max3_f32 v98, v98, v88, v89
	v_max3_f32 v98, v98, v90, v91
	v_max3_f32 v98, v98, v92, v93
	v_max3_f32 v98, v98, v94, v95
	s_waitcnt lgkmcnt(0)
	v_mfma_f32_32x32x16_bf16 v[16:31], v[100:103], v[108:111], v[16:31]
	ds_read_b64_tr_b16 v[108:109], v167 offset:0x200
	ds_read_b64_tr_b16 v[110:111], v167 offset:0xa00
	v_mfma_f32_32x32x16_bf16 v[16:31], v[112:115], v[120:123], v[16:31]
	ds_read_b64_tr_b16 v[120:121], v167 offset:0x1200
	ds_read_b64_tr_b16 v[122:123], v167 offset:0x1a00
	v_mfma_f32_32x32x16_bf16 v[16:31], v[116:119], v[124:127], v[16:31]
	ds_read_b64_tr_b16 v[124:125], v167 offset:0x2200
	ds_read_b64_tr_b16 v[126:127], v167 offset:0x2a00
	ds_read_b64_tr_b16 v[132:133], v167 offset:0x3200
	ds_read_b64_tr_b16 v[134:135], v167 offset:0x3a00
	v_mfma_f32_32x32x16_bf16 v[16:31], v[104:107], v[128:131], v[16:31]
	v_max3_f32 v98, v98, v64, v65
	v_max3_f32 v98, v98, v66, v67
	v_max3_f32 v98, v98, v68, v69
	v_max3_f32 v98, v98, v70, v71
	v_max3_f32 v98, v98, v72, v73
	v_max3_f32 v98, v98, v74, v75
	v_max3_f32 v98, v98, v76, v77
	v_max3_f32 v98, v98, v78, v79
	v_mov_b32_e32 v99, v98
	s_nop 1
	v_permlane32_swap_b32_e32 v98, v99
	v_max_f32_e32 v99, v99, v99
	v_max_f32_e32 v98, v98, v98
	v_max_f32_e32 v98, v98, v99
	v_max_f32_e32 v99, v198, v198
	v_max_f32_e32 v99, v99, v98
	v_sub_f32_e32 v128, v98, v198
	v_sub_f32_e32 v98, v198, v99
	v_mul_f32_e32 v98, 0x3dd53b94, v98
	v_exp_f32_e32 v98, v98
	v_cmp_ge_f32_e32 vcc, s48, v128
	s_cmp_eq_u64 vcc, exec
	s_cselect_b64 s[6:7], -1, 0
	v_cndmask_b32_e64 v98, v98, 1.0, s[6:7]
	s_waitcnt lgkmcnt(0)
	v_mfma_f32_32x32x16_bf16 v[32:47], v[100:103], v[108:111], v[32:47]
	ds_read_b64_tr_b16 v[108:109], v167 offset:0x400
	ds_read_b64_tr_b16 v[110:111], v167 offset:0xc00
	v_mfma_f32_32x32x16_bf16 v[32:47], v[112:115], v[120:123], v[32:47]
	ds_read_b64_tr_b16 v[120:121], v167 offset:0x1400
	ds_read_b64_tr_b16 v[122:123], v167 offset:0x1c00
	v_mfma_f32_32x32x16_bf16 v[32:47], v[116:119], v[124:127], v[32:47]
	ds_read_b64_tr_b16 v[124:125], v167 offset:0x2400
	ds_read_b64_tr_b16 v[126:127], v167 offset:0x2c00
	ds_read_b64_tr_b16 v[128:129], v167 offset:0x3400
	ds_read_b64_tr_b16 v[130:131], v167 offset:0x3c00
	v_mfma_f32_32x32x16_bf16 v[32:47], v[104:107], v[132:135], v[32:47]
	s_waitcnt lgkmcnt(0)
	v_mfma_f32_32x32x16_bf16 v[0:15], v[100:103], v[108:111], v[0:15]
	ds_read_b64_tr_b16 v[108:109], v167 offset:0x600
	ds_read_b64_tr_b16 v[110:111], v167 offset:0xe00
	v_mfma_f32_32x32x16_bf16 v[0:15], v[112:115], v[120:123], v[0:15]
	ds_read_b64_tr_b16 v[120:121], v167 offset:0x1600
	ds_read_b64_tr_b16 v[122:123], v167 offset:0x1e00
	v_mfma_f32_32x32x16_bf16 v[0:15], v[116:119], v[124:127], v[0:15]
	ds_read_b64_tr_b16 v[124:125], v167 offset:0x2600
	ds_read_b64_tr_b16 v[126:127], v167 offset:0x2e00
	ds_read_b64_tr_b16 v[132:133], v167 offset:0x3600
	ds_read_b64_tr_b16 v[134:135], v167 offset:0x3e00
	v_mfma_f32_32x32x16_bf16 v[0:15], v[104:107], v[128:131], v[0:15]
	s_waitcnt lgkmcnt(0)
	v_mfma_f32_32x32x16_bf16 v[48:63], v[100:103], v[108:111], v[48:63]
	v_cmp_gt_f32_e32 vcc, 1.0, v98
	s_waitcnt vmcnt(0)
	s_barrier
	v_mfma_f32_32x32x16_bf16 v[48:63], v[112:115], v[120:123], v[48:63]
	v_mfma_f32_32x32x16_bf16 v[48:63], v[116:119], v[124:127], v[48:63]
	v_mfma_f32_32x32x16_bf16 v[48:63], v[104:107], v[132:135], v[48:63]
	s_cbranch_vccz .LBB0_771
	s_and_saveexec_b64 s[8:9], s[4:5]
	ds_write_b32 v189, v98 offset:128
	s_or_b64 exec, exec, s[8:9]
	s_waitcnt lgkmcnt(0)
	v_add_u32_e32 v112, s62, v169
	ds_read_b128 v[100:103], v112 offset:224
	ds_read_b128 v[104:107], v112 offset:192
	ds_read_b128 v[108:111], v112 offset:160
	ds_read_b128 v[112:115], v112 offset:128
	s_waitcnt lgkmcnt(3)
	v_pk_mul_f32 v[28:29], v[28:29], v[100:101]
	s_waitcnt lgkmcnt(2)
	v_pk_mul_f32 v[24:25], v[24:25], v[104:105]
	s_waitcnt lgkmcnt(1)
	v_pk_mul_f32 v[20:21], v[20:21], v[108:109]
	v_pk_mul_f32 v[30:31], v[30:31], v[102:103]
	v_pk_mul_f32 v[26:27], v[26:27], v[106:107]
	v_pk_mul_f32 v[22:23], v[22:23], v[110:111]
	s_waitcnt lgkmcnt(0)
	v_pk_mul_f32 v[18:19], v[18:19], v[114:115]
	v_pk_mul_f32 v[16:17], v[16:17], v[112:113]
	v_pk_mul_f32 v[44:45], v[44:45], v[100:101]
	v_pk_mul_f32 v[40:41], v[40:41], v[104:105]
	v_pk_mul_f32 v[36:37], v[36:37], v[108:109]
	v_pk_mul_f32 v[46:47], v[46:47], v[102:103]
	v_pk_mul_f32 v[42:43], v[42:43], v[106:107]
	v_pk_mul_f32 v[38:39], v[38:39], v[110:111]
	v_pk_mul_f32 v[34:35], v[34:35], v[114:115]
	v_pk_mul_f32 v[32:33], v[32:33], v[112:113]
	v_pk_mul_f32 v[12:13], v[12:13], v[100:101]
	v_pk_mul_f32 v[8:9], v[8:9], v[104:105]
	v_pk_mul_f32 v[4:5], v[4:5], v[108:109]
	v_pk_mul_f32 v[14:15], v[14:15], v[102:103]
	v_pk_mul_f32 v[10:11], v[10:11], v[106:107]
	v_pk_mul_f32 v[6:7], v[6:7], v[110:111]
	v_pk_mul_f32 v[2:3], v[2:3], v[114:115]
	v_pk_mul_f32 v[0:1], v[0:1], v[112:113]
	v_pk_mul_f32 v[60:61], v[60:61], v[100:101]
	v_pk_mul_f32 v[56:57], v[56:57], v[104:105]
	v_pk_mul_f32 v[52:53], v[52:53], v[108:109]
	v_pk_mul_f32 v[62:63], v[62:63], v[102:103]
	v_pk_mul_f32 v[58:59], v[58:59], v[106:107]
	v_pk_mul_f32 v[54:55], v[54:55], v[110:111]
	v_pk_mul_f32 v[50:51], v[50:51], v[114:115]
	v_pk_mul_f32 v[48:49], v[48:49], v[112:113]

.LBB0_2011:
	s_ashr_i32 s6, s11, 3
	s_lshl_b32 s60, s6, 8
	s_lshl_b32 s61, s6, 12
	s_lshl_b32 s6, s10, 8
	s_and_b32 s6, s6, 0xf00
	s_or_b32 s28, s61, s6
	s_add_i32 s8, s60, 0x4000
	s_and_b32 s12, s11, 7
	s_ashr_i32 s29, s28, 31
	s_mul_i32 s7, s28, 0xc00
	s_mul_hi_i32 s6, s28, 0xc00
	s_add_u32 s7, s35, s7
	s_addc_u32 s6, s36, s6
	s_mul_i32 s13, s12, 0x180
	s_add_u32 s10, s7, s13
	s_addc_u32 s11, s6, 0
	s_add_u32 s6, s37, s13
	s_addc_u32 s7, s38, 0
	s_lshl_b32 s59, s12, 7
	s_lshl_b32 s12, s12, 8
	s_add_u32 s30, s39, s12
	v_readfirstlane_b32 s62, v254
	s_addc_u32 s31, s40, 0
	s_ashr_i32 s12, s62, 6
	s_lshl_b32 s82, s12, 10
	s_mov_b32 s72, s6
	s_and_b32 s73, s7, 0xffff
	s_mov_b32 s74, 0x7ffffff0
	s_mov_b32 s75, 0x20000
	s_mov_b32 s76, s30
	s_and_b32 s77, s31, 0xffff
	s_mov_b32 s78, 0x7ffffff0
	s_mov_b32 s79, 0x20000
	v_ashrrev_i32_e32 v142, 4, v254
	v_mov_b32_e32 v143, 0
	v_ashrrev_i32_e32 v144, 3, v254
	v_mov_b32_e32 v145, 0
	v_add_u32_e32 v146, 32, v142
	v_mov_b32_e32 v147, 0
	v_bfe_u32 v148, v254, 5, 1
	v_lshlrev_b32_e32 v148, 4, v148
	v_mov_b32_e32 v149, 0
	v_and_b32_e32 v150, 15, v254
	v_lshlrev_b32_e32 v150, 4, v150
	v_mov_b32_e32 v151, 0
	v_and_b32_e32 v152, 7, v254
	v_lshlrev_b32_e32 v152, 4, v152
	v_mov_b32_e32 v153, 0
	v_lshl_add_u64 v[26:27], s[8:9], 0, v[142:143]
	v_lshl_add_u64 v[28:29], v[146:147], 0, s[8:9]
	v_lshl_or_b32 v2, s12, 5, v188
	v_mov_b64_e32 v[0:1], s[10:11]
	v_lshlrev_b64 v[16:17], 11, v[26:27]
	v_lshlrev_b64 v[18:19], 11, v[28:29]
	v_mad_i64_i32 v[0:1], s[10:11], v2, s44, v[0:1]
	v_lshl_add_u64 v[16:17], s[30:31], 0, v[16:17]
	v_lshl_add_u64 v[18:19], s[30:31], 0, v[18:19]
	v_lshl_add_u64 v[38:39], v[0:1], 0, v[148:149]
	v_lshl_add_u64 v[16:17], v[16:17], 0, v[150:151]
	v_lshl_add_u64 v[22:23], v[18:19], 0, v[150:151]
	global_load_dwordx4 v[0:3], v[38:39], off offset:256
	global_load_dwordx4 v[4:7], v[38:39], off offset:288
	global_load_dwordx4 v[8:11], v[38:39], off offset:320
	global_load_dwordx4 v[12:15], v[38:39], off offset:352
	global_load_dwordx4 v[18:21], v[16:17], off
	s_nop 0
	global_load_dwordx4 v[22:25], v[22:23], off
	v_mov_b64_e32 v[16:17], s[6:7]
	v_mad_u64_u32 v[30:31], s[10:11], v26, s44, v[16:17]
	v_mad_i32_i24 v31, v27, s44, v31
	v_lshl_add_u64 v[26:27], v[30:31], 0, v[150:151]
	v_mad_u64_u32 v[30:31], s[10:11], v28, s44, v[16:17]
	v_mad_i32_i24 v31, v29, s44, v31
	v_lshl_add_u64 v[30:31], v[30:31], 0, v[150:151]
	v_lshl_add_u64 v[34:35], s[8:9], 0, v[144:145]
	global_load_dwordx4 v[26:29], v[26:27], off
	s_nop 0
	global_load_dwordx4 v[30:33], v[30:31], off
	v_mad_u64_u32 v[36:37], s[10:11], v34, s44, v[16:17]
	v_mad_i32_i24 v37, v35, s44, v37
	v_lshl_add_u64 v[34:35], v[36:37], 0, v[152:153]
	global_load_dwordx4 v[34:37], v[34:35], off offset:256
	s_nop 0
	global_load_dwordx4 v[124:127], v[38:39], off
	global_load_dwordx4 v[120:123], v[38:39], off offset:32
	global_load_dwordx4 v[116:119], v[38:39], off offset:64
	global_load_dwordx4 v[112:115], v[38:39], off offset:96
	global_load_dwordx4 v[108:111], v[38:39], off offset:128
	global_load_dwordx4 v[104:107], v[38:39], off offset:160
	global_load_dwordx4 v[100:103], v[38:39], off offset:192
	global_load_dwordx4 v[96:99], v[38:39], off offset:224
	s_lshl_b32 s8, s12, 12
	v_add_u32_e32 v190, s8, v166
	v_add_u32_e32 v191, s45, v170
	v_add_u32_e32 v192, s45, v171
	v_add_u32_e32 v193, s45, v172
	v_add_u32_e32 v194, s45, v173
	s_mov_b32 s8, s9
	s_mov_b32 s10, s9
	s_mov_b32 s11, s9
	s_mov_b32 s12, s9
	s_mov_b32 s13, s9
	s_mov_b32 s14, s9
	s_mov_b32 s15, s9
	s_mov_b32 s16, s9
	s_mov_b32 s17, s9
	s_mov_b32 s18, s9
	s_mov_b32 s19, s9
	s_mov_b32 s20, s9
	s_mov_b32 s21, s9
	s_mov_b32 s22, s9
	s_mov_b32 s23, s9
	v_add_u32_e32 v195, 0, v168
	v_mov_b32_e32 v140, 0
	v_lshrrev_b32_e32 v156, 4, v254
	v_and_b32_e32 v157, 15, v156
	v_and_b32_e32 v159, 15, v254
	v_xor_b32_e32 v157, v157, v159
	v_lshlrev_b32_e32 v157, 4, v157
	v_mad_u32_u24 v154, v156, s44, v157
	v_lshrrev_b32_e32 v156, 3, v254
	v_bfe_u32 v157, v254, 4, 3
	v_and_b32_e32 v159, 7, v254
	v_xor_b32_e32 v157, v157, v159
	v_lshlrev_b32_e32 v157, 4, v157
	v_add_u32_e32 v157, 0x100, v157
	v_mad_u32_u24 v155, v156, s44, v157
	v_and_b32_e32 v196, 3, v254
	v_lshlrev_b32_e32 v196, 4, v196
	v_bfe_u32 v156, v254, 5, 2
	v_lshl_or_b32 v196, v156, 6, v196
	v_bfe_u32 v156, v254, 2, 2
	v_lshl_or_b32 v196, v156, 11, v196
	v_bfe_u32 v156, v254, 7, 1
	v_lshl_or_b32 v196, v156, 13, v196
	v_bfe_u32 v156, v254, 4, 1
	v_lshl_or_b32 v196, v156, 14, v196
	v_bfe_u32 v156, v254, 8, 1
	v_lshl_or_b32 v196, v156, 15, v196
	v_add_u32_e32 v157, 0x12000, v195
	s_waitcnt vmcnt(16)
	ds_write_b128 v190, v[0:3]
	s_waitcnt vmcnt(15)
	ds_write_b128 v190, v[4:7] offset:1024
	s_waitcnt vmcnt(14)
	ds_write_b128 v190, v[8:11] offset:2048
	s_waitcnt vmcnt(13)
	ds_write_b128 v190, v[12:15] offset:3072
	s_waitcnt vmcnt(0)
	s_waitcnt vmcnt(12)
	ds_write_b128 v175, v[18:21]
	s_waitcnt vmcnt(11)
	ds_write_b128 v176, v[22:25]
	s_waitcnt vmcnt(10)
	ds_write_b128 v177, v[26:29] offset:32768
	s_waitcnt vmcnt(9)
	ds_write_b128 v178, v[30:33] offset:32768
	s_waitcnt vmcnt(8)
	ds_write_b128 v179, v[34:37]
	s_waitcnt lgkmcnt(0)
	s_barrier
	ds_read_b128 v[0:3], v180 offset:32768
	ds_read_b128 v[4:7], v180 offset:40960
	s_waitcnt vmcnt(7) lgkmcnt(1)
	v_mfma_f32_32x32x16_bf16 v[48:63], v[0:3], v[124:127], 0
	s_waitcnt lgkmcnt(0)
	v_mfma_f32_32x32x16_bf16 v[64:79], v[4:7], v[124:127], 0
	ds_read_b128 v[0:3], v181 offset:32768
	ds_read_b128 v[4:7], v181 offset:40960
	s_waitcnt vmcnt(6) lgkmcnt(1)
	v_mfma_f32_32x32x16_bf16 v[48:63], v[0:3], v[120:123], v[48:63]
	s_waitcnt lgkmcnt(0)
	v_mfma_f32_32x32x16_bf16 v[64:79], v[4:7], v[120:123], v[64:79]
	ds_read_b128 v[0:3], v182 offset:32768
	ds_read_b128 v[4:7], v182 offset:40960
	s_waitcnt vmcnt(5) lgkmcnt(1)
	v_mfma_f32_32x32x16_bf16 v[48:63], v[0:3], v[116:119], v[48:63]
	s_waitcnt lgkmcnt(0)
	v_mfma_f32_32x32x16_bf16 v[64:79], v[4:7], v[116:119], v[64:79]
	ds_read_b128 v[0:3], v183 offset:32768
	ds_read_b128 v[4:7], v183 offset:40960
	s_waitcnt vmcnt(4) lgkmcnt(1)
	v_mfma_f32_32x32x16_bf16 v[48:63], v[0:3], v[112:115], v[48:63]
	s_waitcnt lgkmcnt(0)
	v_mfma_f32_32x32x16_bf16 v[64:79], v[4:7], v[112:115], v[64:79]
	ds_read_b128 v[0:3], v184 offset:32768
	ds_read_b128 v[4:7], v184 offset:40960
	s_waitcnt vmcnt(3) lgkmcnt(1)
	v_mfma_f32_32x32x16_bf16 v[48:63], v[0:3], v[108:111], v[48:63]
	s_waitcnt lgkmcnt(0)
	v_mfma_f32_32x32x16_bf16 v[64:79], v[4:7], v[108:111], v[64:79]
	ds_read_b128 v[0:3], v185 offset:32768
	ds_read_b128 v[4:7], v185 offset:40960
	s_waitcnt vmcnt(2) lgkmcnt(1)
	v_mfma_f32_32x32x16_bf16 v[48:63], v[0:3], v[104:107], v[48:63]
	s_waitcnt lgkmcnt(0)
	v_mfma_f32_32x32x16_bf16 v[64:79], v[4:7], v[104:107], v[64:79]
	ds_read_b128 v[0:3], v186 offset:32768
	ds_read_b128 v[4:7], v186 offset:40960
	s_waitcnt vmcnt(1) lgkmcnt(1)
	v_mfma_f32_32x32x16_bf16 v[48:63], v[0:3], v[100:103], v[48:63]
	s_waitcnt lgkmcnt(0)
	v_mfma_f32_32x32x16_bf16 v[64:79], v[4:7], v[100:103], v[64:79]
	ds_read_b128 v[0:3], v187 offset:32768
	ds_read_b128 v[4:7], v187 offset:40960
	s_waitcnt vmcnt(0) lgkmcnt(1)
	v_mfma_f32_32x32x16_bf16 v[48:63], v[0:3], v[96:99], v[48:63]
	s_waitcnt lgkmcnt(0)
	v_mfma_f32_32x32x16_bf16 v[64:79], v[4:7], v[96:99], v[64:79]
	ds_read_b128 v[0:3], v191
	ds_read_b128 v[4:7], v190
	ds_read_b128 v[8:11], v191 offset:4096
	ds_read_b128 v[12:15], v190 offset:1024
	s_waitcnt lgkmcnt(2)
	v_mfma_f32_32x32x16_bf16 v[48:63], v[0:3], v[4:7], v[48:63]
	s_waitcnt lgkmcnt(1)
	v_mfma_f32_32x32x16_bf16 v[64:79], v[8:11], v[4:7], v[64:79]
	ds_read_b128 v[0:3], v192
	ds_read_b128 v[4:7], v192 offset:4096
	s_waitcnt lgkmcnt(1)
	v_mfma_f32_32x32x16_bf16 v[48:63], v[0:3], v[12:15], v[48:63]
	s_waitcnt lgkmcnt(0)
	v_mfma_f32_32x32x16_bf16 v[64:79], v[4:7], v[12:15], v[64:79]
	ds_read_b128 v[0:3], v193
	ds_read_b128 v[4:7], v190 offset:2048
	ds_read_b128 v[8:11], v193 offset:4096
	ds_read_b128 v[18:21], v190 offset:3072
	ds_read_b128 v[22:25], v194 offset:4096
	s_waitcnt lgkmcnt(3)
	v_mfma_f32_32x32x16_bf16 v[48:63], v[0:3], v[4:7], v[48:63]
	ds_read_b128 v[0:3], v194
	s_waitcnt lgkmcnt(3)
	v_mfma_f32_32x32x16_bf16 v[64:79], v[8:11], v[4:7], v[64:79]
	s_waitcnt lgkmcnt(0)
	v_mfma_f32_32x32x16_bf16 v[48:63], v[0:3], v[18:21], v[48:63]
	v_mov_b64_e32 v[0:1], s[8:9]
	v_mov_b64_e32 v[2:3], s[10:11]
	v_mov_b64_e32 v[4:5], s[12:13]
	v_mov_b64_e32 v[6:7], s[14:15]
	v_mov_b64_e32 v[8:9], s[16:17]
	v_mov_b64_e32 v[10:11], s[18:19]
	v_mov_b64_e32 v[12:13], s[20:21]
	v_mfma_f32_32x32x16_bf16 v[64:79], v[22:25], v[18:21], v[64:79]
	s_nop 3
	v_max_f32_e32 v18, v49, v49
	v_max_f32_e32 v19, v48, v48
	v_max_f32_e32 v18, v19, v18
	v_max3_f32 v18, v18, v50, v51
	v_max3_f32 v18, v18, v52, v53
	v_max3_f32 v18, v18, v54, v55
	v_max3_f32 v18, v18, v56, v57
	v_max3_f32 v18, v18, v58, v59
	v_max3_f32 v18, v18, v60, v61
	v_max3_f32 v18, v18, v62, v63
	v_max3_f32 v18, v18, v64, v65
	v_max3_f32 v18, v18, v66, v67
	v_max3_f32 v18, v18, v68, v69
	v_max3_f32 v18, v18, v70, v71
	v_max3_f32 v18, v18, v72, v73
	v_max3_f32 v18, v18, v74, v75
	v_max3_f32 v18, v18, v76, v77
	v_max3_f32 v18, v18, v78, v79
	v_mov_b32_e32 v19, v18
	s_nop 1
	v_permlane32_swap_b32_e32 v18, v19
	v_mov_b64_e32 v[14:15], s[22:23]
	s_and_b32 s8, s62, 0x3fffffc0
	v_max_f32_e32 v19, v19, v19
	v_max_f32_e32 v18, v18, v18
	s_lshl_b32 s8, s8, 2
	v_max_f32_e32 v18, v18, v19
	s_add_i32 s12, s8, 0
	v_add_f32_e32 v19, 0x7149f2ca, v18
	s_add_i32 s12, s12, 0x14000
	v_cmp_ge_f32_e32 vcc, s46, v19
	s_cmp_eq_u64 vcc, exec
	s_cselect_b64 vcc, -1, 0
	s_add_i32 s8, s60, 0x4040
	v_max_f32_e32 v128, 0xf149f2ca, v18
	v_lshl_add_u64 v[18:19], s[8:9], 0, v[142:143]
	v_lshl_add_u64 v[20:21], v[146:147], 0, s[8:9]
	v_lshl_add_u64 v[22:23], s[8:9], 0, v[144:145]
	v_lshlrev_b64 v[24:25], 11, v[18:19]
	v_lshlrev_b64 v[26:27], 11, v[20:21]
	v_mad_u64_u32 v[28:29], s[10:11], v18, s44, v[16:17]
	v_mad_u64_u32 v[30:31], s[10:11], v20, s44, v[16:17]
	v_mad_u64_u32 v[16:17], s[10:11], v22, s44, v[16:17]
	v_lshl_add_u64 v[24:25], s[30:31], 0, v[24:25]
	v_lshl_add_u64 v[26:27], s[30:31], 0, v[26:27]
	v_mad_i32_i24 v29, v19, s44, v29
	v_mad_i32_i24 v31, v21, s44, v31
	v_mad_i32_i24 v17, v23, s44, v17
	v_lshl_add_u64 v[18:19], v[24:25], 0, v[150:151]
	v_lshl_add_u64 v[20:21], v[26:27], 0, v[150:151]
	v_lshl_add_u64 v[22:23], v[28:29], 0, v[150:151]
	v_lshl_add_u64 v[24:25], v[30:31], 0, v[150:151]
	v_lshl_add_u64 v[16:17], v[16:17], 0, v[152:153]
	global_load_dwordx4 v[80:83], v[18:19], off
	global_load_dwordx4 v[84:87], v[20:21], off
	global_load_dwordx4 v[88:91], v[22:23], off
	global_load_dwordx4 v[92:95], v[24:25], off
	global_load_dwordx4 v[200:203], v[16:17], off offset:256
	v_sub_f32_e32 v129, 0xf149f2ca, v128
	v_mul_f32_e32 v129, 0x3dd53b94, v129
	v_exp_f32_e32 v164, v129
	v_mov_b32_e32 v129, 0xf149f2ca
	v_cndmask_b32_e32 v198, v128, v129, vcc
	v_mul_f32_e32 v138, 0xbdd53b94, v198
	v_mov_b32_e32 v165, v138
	v_fmamk_f32 v48, v48, 0x3dd53b94, v138
	v_fmamk_f32 v49, v49, 0x3dd53b94, v138
	v_fmamk_f32 v50, v50, 0x3dd53b94, v138
	v_fmamk_f32 v51, v51, 0x3dd53b94, v138
	v_fmamk_f32 v52, v52, 0x3dd53b94, v138
	v_fmamk_f32 v53, v53, 0x3dd53b94, v138
	v_fmamk_f32 v54, v54, 0x3dd53b94, v138
	v_fmamk_f32 v55, v55, 0x3dd53b94, v138
	v_fmamk_f32 v56, v56, 0x3dd53b94, v138
	v_fmamk_f32 v57, v57, 0x3dd53b94, v138
	v_fmamk_f32 v58, v58, 0x3dd53b94, v138
	v_fmamk_f32 v59, v59, 0x3dd53b94, v138
	v_fmamk_f32 v60, v60, 0x3dd53b94, v138
	v_fmamk_f32 v61, v61, 0x3dd53b94, v138
	v_fmamk_f32 v62, v62, 0x3dd53b94, v138
	v_fmac_f32_e32 v165, 0x3dd53b94, v63
	v_exp_f32_e32 v222, v48
	v_exp_f32_e32 v224, v49
	v_exp_f32_e32 v220, v50
	v_exp_f32_e32 v223, v51
	v_exp_f32_e32 v219, v52
	v_exp_f32_e32 v221, v53
	v_exp_f32_e32 v217, v54
	v_exp_f32_e32 v218, v55
	v_exp_f32_e32 v212, v56
	v_exp_f32_e32 v214, v57
	v_exp_f32_e32 v211, v58
	v_exp_f32_e32 v213, v59
	v_exp_f32_e32 v208, v60
	v_exp_f32_e32 v210, v61
	v_exp_f32_e32 v207, v62
	v_exp_f32_e32 v209, v165
	s_waitcnt vmcnt(0)
	v_mov_b64_e32 v[46:47], v[14:15]
	v_mov_b64_e32 v[30:31], v[14:15]
	v_mov_b64_e32 v[62:63], v[14:15]
	s_mov_b32 s8, -1
	v_mov_b64_e32 v[44:45], v[12:13]
	v_mov_b64_e32 v[42:43], v[10:11]
	v_mov_b64_e32 v[40:41], v[8:9]
	v_mov_b64_e32 v[38:39], v[6:7]
	v_mov_b64_e32 v[36:37], v[4:5]
	v_mov_b64_e32 v[34:35], v[2:3]
	v_mov_b64_e32 v[32:33], v[0:1]
	v_mov_b64_e32 v[28:29], v[12:13]
	v_mov_b64_e32 v[26:27], v[10:11]
	v_mov_b64_e32 v[24:25], v[8:9]
	v_mov_b64_e32 v[22:23], v[6:7]
	v_mov_b64_e32 v[20:21], v[4:5]
	v_mov_b64_e32 v[18:19], v[2:3]
	v_mov_b64_e32 v[16:17], v[0:1]
	v_lshl_add_u32 v189, v188, 2, s12
	s_add_i32 s13, s60, 0x4080
	s_add_i32 s83, s60, 0x4040
	s_sub_i32 s14, s61, 64
	v_pk_fma_f32 v[134:135], v[78:79], s[26:27], v[138:139] op_sel_hi:[1,0,0]
	v_pk_fma_f32 v[160:161], v[76:77], s[26:27], v[138:139] op_sel_hi:[1,0,0]
	v_pk_fma_f32 v[162:163], v[74:75], s[26:27], v[138:139] op_sel_hi:[1,0,0]
	v_pk_fma_f32 v[128:129], v[72:73], s[26:27], v[138:139] op_sel_hi:[1,0,0]
	v_pk_fma_f32 v[130:131], v[70:71], s[26:27], v[138:139] op_sel_hi:[1,0,0]
	v_pk_fma_f32 v[132:133], v[68:69], s[26:27], v[138:139] op_sel_hi:[1,0,0]
	v_pk_fma_f32 v[136:137], v[66:67], s[26:27], v[138:139] op_sel_hi:[1,0,0]
	v_pk_fma_f32 v[138:139], v[64:65], s[26:27], v[138:139] op_sel_hi:[1,0,0]
	v_cndmask_b32_e64 v197, v164, 1.0, vcc
	v_mov_b64_e32 v[60:61], v[12:13]
	v_mov_b64_e32 v[58:59], v[10:11]
	v_mov_b64_e32 v[56:57], v[8:9]
	v_mov_b64_e32 v[54:55], v[6:7]
	v_mov_b64_e32 v[52:53], v[4:5]
	v_mov_b64_e32 v[50:51], v[2:3]
	v_mov_b64_e32 v[48:49], v[0:1]
	s_waitcnt vmcnt(4)
	ds_write_b128 v175, v[80:83] offset:16384
	s_waitcnt vmcnt(3)
	ds_write_b128 v176, v[84:87] offset:16384
	s_waitcnt vmcnt(2)
	ds_write_b128 v177, v[88:91] offset:49152
	s_waitcnt vmcnt(1)
	ds_write_b128 v178, v[92:95] offset:49152
	s_waitcnt vmcnt(0)
	ds_write_b128 v157, v[200:203]
	ds_read_b128 v[142:145], v190
	ds_read_b128 v[146:149], v190 offset:1024
	ds_read_b128 v[150:153], v190 offset:2048
	ds_read_b128 v[156:159], v190 offset:3072
	s_waitcnt lgkmcnt(0)
	s_barrier
.LBB0_2012:
	s_add_i32 s8, s8, 2
	s_sub_i32 s80, s14, 64
	s_cmp_lt_u32 s8, 3
	s_cselect_b32 s80, s13, s80
	s_mul_i32 s81, s80, 0xc00
	s_add_i32 s85, s82, 0x8000
	s_mov_b32 m0, s85
	s_add_i32 s85, s82, 0x10000
	buffer_load_dwordx4 v154, s[72:75], s81 offen lds
	s_mov_b32 m0, s85
	s_add_i32 s85, s82, 0xa000
	buffer_load_dwordx4 v155, s[72:75], s81 offen lds
	s_mov_b32 m0, s85
	s_add_i32 s81, s81, 0x18000
	buffer_load_dwordx4 v154, s[72:75], s81 offen lds
	s_lshl_b32 s81, s83, 11
	s_add_i32 s85, s82, 0x4000
	s_mov_b32 m0, s85
	s_add_i32 s85, s82, 0x6000
	buffer_load_dwordx4 v196, s[76:79], s81 offen lds
	s_mov_b32 m0, s85
	s_add_i32 s81, s81, 0x10000
	buffer_load_dwordx4 v196, s[76:79], s81 offen lds
	s_mov_b32 s84, s80
	s_add_i32 s6, 0, 0x12000
	v_add_u32_e32 v199, s6, v170
	v_add_u32_e32 v204, s6, v171
	v_add_u32_e32 v205, s6, v172
	ds_read_b128 v[64:67], v180 offset:49152
	ds_read_b128 v[68:71], v180 offset:57344
	ds_read_b128 v[200:203], v181 offset:49152
	ds_read_b128 v[226:229], v181 offset:57344
	ds_read_b128 v[230:233], v182 offset:49152
	ds_read_b128 v[234:237], v182 offset:57344
	ds_read_b128 v[238:241], v183 offset:49152
	ds_read_b128 v[242:245], v183 offset:57344
	s_waitcnt lgkmcnt(7)
	v_mfma_f32_32x32x16_bf16 v[80:95], v[64:67], v[124:127], 0
	v_exp_f32_e32 v216, v128
	v_add_f32_e32 v128, 0, v222
	v_add_f32_e32 v128, v224, v128
	v_add_f32_e32 v128, v220, v128
	v_add_f32_e32 v128, v223, v128
	v_add_f32_e32 v128, v219, v128
	v_add_f32_e32 v128, v221, v128
	s_waitcnt lgkmcnt(6)
	v_mfma_f32_32x32x16_bf16 v[64:79], v[68:71], v[124:127], 0
	v_add_f32_e32 v128, v217, v128
	v_add_f32_e32 v128, v218, v128
	v_add_f32_e32 v128, v212, v128
	v_add_f32_e32 v128, v214, v128
	v_add_f32_e32 v128, v211, v128
	v_add_f32_e32 v128, v213, v128
	v_exp_f32_e32 v138, v138
	s_waitcnt lgkmcnt(5)
	v_mfma_f32_32x32x16_bf16 v[80:95], v[200:203], v[120:123], v[80:95]
	v_add_f32_e32 v128, v208, v128
	v_exp_f32_e32 v139, v139
	v_add_f32_e32 v128, v210, v128
	v_exp_f32_e32 v164, v136
	v_add_f32_e32 v128, v207, v128
	v_exp_f32_e32 v137, v137
	v_add_f32_e32 v128, v209, v128
	s_waitcnt lgkmcnt(4)
	v_mfma_f32_32x32x16_bf16 v[64:79], v[226:229], v[120:123], v[64:79]
	ds_read_b128 v[200:203], v184 offset:49152
	ds_read_b128 v[226:229], v184 offset:57344
	v_exp_f32_e32 v165, v132
	v_add_f32_e32 v128, v138, v128
	v_add_f32_e32 v128, v139, v128
	v_exp_f32_e32 v206, v130
	v_add_f32_e32 v128, v164, v128
	v_exp_f32_e32 v215, v131
	s_waitcnt lgkmcnt(5)
	v_mfma_f32_32x32x16_bf16 v[80:95], v[230:233], v[116:119], v[80:95]
	v_add_f32_e32 v128, v137, v128
	v_add_f32_e32 v128, v165, v128
	v_exp_f32_e32 v225, v129
	v_exp_f32_e32 v162, v162
	v_exp_f32_e32 v163, v163
	v_exp_f32_e32 v160, v160
	v_exp_f32_e32 v161, v161
	s_waitcnt lgkmcnt(4)
	v_mfma_f32_32x32x16_bf16 v[64:79], v[234:237], v[116:119], v[64:79]
	ds_read_b128 v[230:233], v185 offset:49152
	ds_read_b128 v[234:237], v185 offset:57344
	v_cvt_pk_bf16_f32 v129, v220, v223
	v_cvt_pk_bf16_f32 v130, v219, v221
	v_cvt_pk_bf16_f32 v131, v217, v218
	v_cvt_pk_bf16_f32 v132, v212, v214
	v_cvt_pk_bf16_f32 v136, v138, v139
	v_cvt_pk_bf16_f32 v137, v164, v137
	s_waitcnt lgkmcnt(5)
	v_mfma_f32_32x32x16_bf16 v[80:95], v[238:241], v[112:115], v[80:95]
	v_cvt_pk_bf16_f32 v139, v206, v215
	v_permlane32_swap_b32_e32 v129, v131
	s_nop 0
	v_permlane32_swap_b32_e32 v137, v139
	s_waitcnt lgkmcnt(4)
	v_mfma_f32_32x32x16_bf16 v[64:79], v[242:245], v[112:115], v[64:79]
	ds_read_b128 v[238:241], v186 offset:49152
	ds_read_b128 v[242:245], v186 offset:57344
	s_waitcnt lgkmcnt(5)
	v_mfma_f32_32x32x16_bf16 v[80:95], v[200:203], v[108:111], v[80:95]
	s_waitcnt lgkmcnt(4)
	v_mfma_f32_32x32x16_bf16 v[64:79], v[226:229], v[108:111], v[64:79]
	ds_read_b128 v[200:203], v187 offset:49152
	ds_read_b128 v[226:229], v187 offset:57344
	s_waitcnt lgkmcnt(5)
	v_mfma_f32_32x32x16_bf16 v[80:95], v[230:233], v[104:107], v[80:95]
	s_waitcnt lgkmcnt(4)
	v_mfma_f32_32x32x16_bf16 v[64:79], v[234:237], v[104:107], v[64:79]
	ds_read_b128 v[230:233], v199
	ds_read_b128 v[234:237], v199 offset:4096
	s_waitcnt lgkmcnt(5)
	v_mfma_f32_32x32x16_bf16 v[80:95], v[238:241], v[100:103], v[80:95]
	s_waitcnt lgkmcnt(4)
	v_mfma_f32_32x32x16_bf16 v[64:79], v[242:245], v[100:103], v[64:79]
	ds_read_b128 v[238:241], v204
	ds_read_b128 v[242:245], v204 offset:4096
	v_add_u32_e32 v204, s6, v173
	s_waitcnt lgkmcnt(5)
	v_mfma_f32_32x32x16_bf16 v[80:95], v[200:203], v[96:99], v[80:95]
	s_waitcnt lgkmcnt(4)
	v_mfma_f32_32x32x16_bf16 v[64:79], v[226:229], v[96:99], v[64:79]
	ds_read_b128 v[200:203], v205
	ds_read_b128 v[226:229], v205 offset:4096
	s_waitcnt lgkmcnt(5)
	v_mfma_f32_32x32x16_bf16 v[80:95], v[230:233], v[142:145], v[80:95]
	s_waitcnt lgkmcnt(4)
	v_mfma_f32_32x32x16_bf16 v[64:79], v[234:237], v[142:145], v[64:79]
	ds_read_b128 v[230:233], v204
	ds_read_b128 v[234:237], v204 offset:4096
	s_waitcnt lgkmcnt(5)
	v_mfma_f32_32x32x16_bf16 v[80:95], v[238:241], v[146:149], v[80:95]
	s_waitcnt lgkmcnt(4)
	v_mfma_f32_32x32x16_bf16 v[64:79], v[242:245], v[146:149], v[64:79]
	s_waitcnt lgkmcnt(3)
	v_mfma_f32_32x32x16_bf16 v[80:95], v[200:203], v[150:153], v[80:95]
	v_exp_f32_e32 v205, v133
	v_cvt_pk_bf16_f32 v133, v211, v213
	v_cvt_pk_bf16_f32 v138, v165, v205
	v_add_f32_e32 v128, v205, v128
	v_add_f32_e32 v128, v206, v128
	v_add_f32_e32 v128, v215, v128
	s_waitcnt lgkmcnt(2)
	v_mfma_f32_32x32x16_bf16 v[64:79], v[226:229], v[150:153], v[64:79]
	v_add_f32_e32 v128, v216, v128
	v_add_f32_e32 v128, v225, v128
	v_add_f32_e32 v128, v162, v128
	v_add_f32_e32 v128, v163, v128
	v_add_f32_e32 v128, v160, v128
	v_add_f32_e32 v128, v161, v128
	s_waitcnt lgkmcnt(1)
	v_mfma_f32_32x32x16_bf16 v[80:95], v[230:233], v[156:159], v[80:95]
	v_exp_f32_e32 v226, v134
	v_exp_f32_e32 v227, v135
	v_cvt_pk_bf16_f32 v134, v208, v210
	v_cvt_pk_bf16_f32 v135, v207, v209
	v_add_f32_e32 v128, v226, v128
	v_add_f32_e32 v203, v227, v128
	v_mov_b32_e32 v204, v203
	s_waitcnt lgkmcnt(0)
	v_mfma_f32_32x32x16_bf16 v[64:79], v[234:237], v[156:159], v[64:79]
	s_nop 0
	v_permlane32_swap_b32_e32 v203, v204
	v_cvt_pk_bf16_f32 v128, v222, v224
	v_cvt_pk_bf16_f32 v208, v216, v225
	v_cvt_pk_bf16_f32 v209, v162, v163
	v_cvt_pk_bf16_f32 v210, v160, v161
	v_cvt_pk_bf16_f32 v211, v226, v227
	v_permlane32_swap_b32_e32 v132, v134
	v_permlane32_swap_b32_e32 v128, v130
	v_permlane32_swap_b32_e32 v133, v135
	v_permlane32_swap_b32_e32 v136, v138
	v_permlane32_swap_b32_e32 v208, v210
	v_permlane32_swap_b32_e32 v209, v211
	ds_read_b64_tr_b16 v[160:161], v167 offset:0
	ds_read_b64_tr_b16 v[162:163], v167 offset:0x800
	ds_read_b64_tr_b16 v[232:233], v167 offset:0x1000
	ds_read_b64_tr_b16 v[234:235], v167 offset:0x1800
	ds_read_b64_tr_b16 v[236:237], v167 offset:0x2000
	ds_read_b64_tr_b16 v[238:239], v167 offset:0x2800
	ds_read_b64_tr_b16 v[240:241], v167 offset:0x3000
	ds_read_b64_tr_b16 v[242:243], v167 offset:0x3800
	v_max_f32_e32 v164, v81, v81
	v_max_f32_e32 v165, v80, v80
	v_max_f32_e32 v164, v165, v164
	v_max3_f32 v164, v164, v82, v83
	v_max3_f32 v164, v164, v84, v85
	v_max3_f32 v164, v164, v86, v87
	v_max3_f32 v164, v164, v88, v89
	v_max3_f32 v164, v164, v90, v91
	v_max3_f32 v164, v164, v92, v93
	v_max3_f32 v164, v164, v94, v95
	s_waitcnt lgkmcnt(0)
	v_mfma_f32_32x32x16_bf16 v[0:15], v[128:131], v[160:163], v[0:15]
	v_max3_f32 v160, v164, v64, v65
	v_max3_f32 v160, v160, v66, v67
	v_max3_f32 v160, v160, v68, v69
	v_mfma_f32_32x32x16_bf16 v[0:15], v[132:135], v[232:235], v[0:15]
	ds_read_b64_tr_b16 v[232:233], v167 offset:0x200
	ds_read_b64_tr_b16 v[234:235], v167 offset:0xa00
	v_max3_f32 v160, v160, v70, v71
	v_max3_f32 v160, v160, v72, v73
	v_max3_f32 v160, v160, v74, v75
	v_mfma_f32_32x32x16_bf16 v[0:15], v[136:139], v[236:239], v[0:15]
	ds_read_b64_tr_b16 v[236:237], v167 offset:0x1200
	ds_read_b64_tr_b16 v[238:239], v167 offset:0x1a00
	ds_read_b64_tr_b16 v[244:245], v167 offset:0x2200
	ds_read_b64_tr_b16 v[246:247], v167 offset:0x2a00
	ds_read_b64_tr_b16 v[248:249], v167 offset:0x3200
	ds_read_b64_tr_b16 v[250:251], v167 offset:0x3a00
	v_max3_f32 v160, v160, v76, v77
	v_max3_f32 v160, v160, v78, v79
	v_mov_b32_e32 v161, v160
	v_mfma_f32_32x32x16_bf16 v[0:15], v[208:211], v[240:243], v[0:15]
	v_max_f32_e32 v162, v198, v198
	v_permlane32_swap_b32_e32 v160, v161
	v_max_f32_e32 v161, v161, v161
	v_max_f32_e32 v160, v160, v160
	v_max_f32_e32 v160, v160, v161
	s_waitcnt lgkmcnt(0)
	v_mfma_f32_32x32x16_bf16 v[32:47], v[128:131], v[232:235], v[32:47]
	ds_read_b64_tr_b16 v[232:233], v167 offset:0x400
	ds_read_b64_tr_b16 v[234:235], v167 offset:0xc00
	v_sub_f32_e32 v161, v160, v198
	v_max_f32_e32 v160, v162, v160
	v_sub_f32_e32 v162, v198, v160
	v_mul_f32_e32 v162, 0x3dd53b94, v162
	v_exp_f32_e32 v162, v162
	v_mfma_f32_32x32x16_bf16 v[32:47], v[132:135], v[236:239], v[32:47]
	ds_read_b64_tr_b16 v[236:237], v167 offset:0x1400
	ds_read_b64_tr_b16 v[238:239], v167 offset:0x1c00
	ds_read_b64_tr_b16 v[240:241], v167 offset:0x2400
	ds_read_b64_tr_b16 v[242:243], v167 offset:0x2c00
	v_cmp_ge_f32_e32 vcc, s46, v161
	s_cmp_eq_u64 vcc, exec
	s_cselect_b64 s[6:7], -1, 0
	v_cndmask_b32_e64 v206, v162, 1.0, s[6:7]
	v_cndmask_b32_e64 v160, v160, v198, s[6:7]
	v_mul_f32_e32 v205, 0xbdd53b94, v160
	v_cmp_gt_f32_e32 vcc, 1.0, v206
	v_mfma_f32_32x32x16_bf16 v[32:47], v[136:139], v[244:247], v[32:47]
	ds_read_b64_tr_b16 v[244:245], v167 offset:0x3400
	ds_read_b64_tr_b16 v[246:247], v167 offset:0x3c00
	v_fmamk_f32 v87, v87, 0x3dd53b94, v205
	v_fmamk_f32 v80, v80, 0x3dd53b94, v205
	v_fmamk_f32 v81, v81, 0x3dd53b94, v205
	v_fmamk_f32 v82, v82, 0x3dd53b94, v205
	v_fmamk_f32 v83, v83, 0x3dd53b94, v205
	v_mfma_f32_32x32x16_bf16 v[32:47], v[208:211], v[248:251], v[32:47]
	v_fmamk_f32 v84, v84, 0x3dd53b94, v205
	v_fmamk_f32 v85, v85, 0x3dd53b94, v205
	v_fmamk_f32 v86, v86, 0x3dd53b94, v205
	v_fmamk_f32 v88, v88, 0x3dd53b94, v205
	v_fmamk_f32 v89, v89, 0x3dd53b94, v205
	s_waitcnt lgkmcnt(0)
	v_mfma_f32_32x32x16_bf16 v[16:31], v[128:131], v[232:235], v[16:31]
	ds_read_b64_tr_b16 v[232:233], v167 offset:0x600
	ds_read_b64_tr_b16 v[234:235], v167 offset:0xe00
	v_fmamk_f32 v90, v90, 0x3dd53b94, v205
	v_fmamk_f32 v91, v91, 0x3dd53b94, v205
	v_fmamk_f32 v92, v92, 0x3dd53b94, v205
	v_fmamk_f32 v93, v93, 0x3dd53b94, v205
	v_fmamk_f32 v94, v94, 0x3dd53b94, v205
	v_mfma_f32_32x32x16_bf16 v[16:31], v[132:135], v[236:239], v[16:31]
	ds_read_b64_tr_b16 v[236:237], v167 offset:0x1600
	ds_read_b64_tr_b16 v[238:239], v167 offset:0x1e00
	v_fmamk_f32 v95, v95, 0x3dd53b94, v205
	v_fmamk_f32 v215, v64, 0x3dd53b94, v205
	v_fmamk_f32 v216, v65, 0x3dd53b94, v205
	v_fmamk_f32 v217, v66, 0x3dd53b94, v205
	v_fmamk_f32 v218, v67, 0x3dd53b94, v205
	v_mfma_f32_32x32x16_bf16 v[16:31], v[136:139], v[240:243], v[16:31]
	ds_read_b64_tr_b16 v[240:241], v167 offset:0x2600
	ds_read_b64_tr_b16 v[242:243], v167 offset:0x2e00
	ds_read_b64_tr_b16 v[248:249], v167 offset:0x3600
	ds_read_b64_tr_b16 v[250:251], v167 offset:0x3e00
	v_fmamk_f32 v219, v68, 0x3dd53b94, v205
	v_fmamk_f32 v212, v73, 0x3dd53b94, v205
	v_fmamk_f32 v213, v74, 0x3dd53b94, v205
	v_fmamk_f32 v214, v75, 0x3dd53b94, v205
	v_mfma_f32_32x32x16_bf16 v[16:31], v[208:211], v[244:247], v[16:31]
	v_fmamk_f32 v207, v76, 0x3dd53b94, v205
	v_fmamk_f32 v220, v77, 0x3dd53b94, v205
	v_fmamk_f32 v221, v78, 0x3dd53b94, v205
	s_waitcnt lgkmcnt(0)
	v_mfma_f32_32x32x16_bf16 v[48:63], v[128:131], v[232:235], v[48:63]
	v_exp_f32_e32 v128, v80
	v_exp_f32_e32 v129, v82
	v_exp_f32_e32 v130, v84
	v_exp_f32_e32 v131, v86
	v_mfma_f32_32x32x16_bf16 v[48:63], v[132:135], v[236:239], v[48:63]
	v_exp_f32_e32 v132, v88
	v_exp_f32_e32 v133, v90
	v_exp_f32_e32 v134, v92
	v_exp_f32_e32 v135, v94
	v_mfma_f32_32x32x16_bf16 v[48:63], v[136:139], v[240:243], v[48:63]
	v_exp_f32_e32 v139, v89
	v_exp_f32_e32 v138, v91
	v_exp_f32_e32 v137, v93
	v_exp_f32_e32 v136, v95
	v_mfma_f32_32x32x16_bf16 v[48:63], v[208:211], v[248:251], v[48:63]
	v_exp_f32_e32 v161, v87
	v_exp_f32_e32 v198, v81
	v_exp_f32_e32 v163, v83
	v_exp_f32_e32 v162, v85
	v_fmamk_f32 v208, v69, 0x3dd53b94, v205
	v_fmamk_f32 v209, v70, 0x3dd53b94, v205
	v_fmamk_f32 v210, v71, 0x3dd53b94, v205
	v_fmamk_f32 v211, v72, 0x3dd53b94, v205
	v_fmac_f32_e32 v205, 0x3dd53b94, v79
	s_cbranch_vccz .LBB0_2016
	s_and_saveexec_b64 s[10:11], s[4:5]
	ds_write_b32 v189, v206 offset:128
	s_or_b64 exec, exec, s[10:11]
	s_waitcnt lgkmcnt(0)
	v_add_u32_e32 v248, s12, v169
	ds_read_b128 v[232:235], v248 offset:224
	ds_read_b128 v[236:239], v248 offset:192
	ds_read_b128 v[240:243], v248 offset:160
	ds_read_b128 v[244:247], v248 offset:128
	s_waitcnt lgkmcnt(3)
	v_pk_mul_f32 v[12:13], v[12:13], v[232:233]
	s_waitcnt lgkmcnt(2)
	v_pk_mul_f32 v[8:9], v[8:9], v[236:237]
	s_waitcnt lgkmcnt(1)
	v_pk_mul_f32 v[4:5], v[4:5], v[240:241]
	v_pk_mul_f32 v[14:15], v[14:15], v[234:235]
	v_pk_mul_f32 v[10:11], v[10:11], v[238:239]
	v_pk_mul_f32 v[6:7], v[6:7], v[242:243]
	s_waitcnt lgkmcnt(0)
	v_pk_mul_f32 v[2:3], v[2:3], v[246:247]
	v_pk_mul_f32 v[0:1], v[0:1], v[244:245]
	v_pk_mul_f32 v[44:45], v[44:45], v[232:233]
	v_pk_mul_f32 v[40:41], v[40:41], v[236:237]
	v_pk_mul_f32 v[36:37], v[36:37], v[240:241]
	v_pk_mul_f32 v[46:47], v[46:47], v[234:235]
	v_pk_mul_f32 v[42:43], v[42:43], v[238:239]
	v_pk_mul_f32 v[38:39], v[38:39], v[242:243]
	v_pk_mul_f32 v[34:35], v[34:35], v[246:247]
	v_pk_mul_f32 v[32:33], v[32:33], v[244:245]
	v_pk_mul_f32 v[28:29], v[28:29], v[232:233]
	v_pk_mul_f32 v[24:25], v[24:25], v[236:237]
	v_pk_mul_f32 v[20:21], v[20:21], v[240:241]
	v_pk_mul_f32 v[30:31], v[30:31], v[234:235]
	v_pk_mul_f32 v[26:27], v[26:27], v[238:239]
	v_pk_mul_f32 v[22:23], v[22:23], v[242:243]
	v_pk_mul_f32 v[18:19], v[18:19], v[246:247]
	v_pk_mul_f32 v[16:17], v[16:17], v[244:245]
	v_pk_mul_f32 v[60:61], v[60:61], v[232:233]
	v_pk_mul_f32 v[56:57], v[56:57], v[236:237]
	v_pk_mul_f32 v[52:53], v[52:53], v[240:241]
	v_pk_mul_f32 v[62:63], v[62:63], v[234:235]
	v_pk_mul_f32 v[58:59], v[58:59], v[238:239]
	v_pk_mul_f32 v[54:55], v[54:55], v[242:243]
	v_pk_mul_f32 v[50:51], v[50:51], v[246:247]
	v_pk_mul_f32 v[48:49], v[48:49], v[244:245]
.LBB0_2016:
	s_waitcnt vmcnt(0) lgkmcnt(0)
	s_barrier
	s_add_i32 s80, s13, 64
	s_cmp_lt_u32 s8, 2
	s_cselect_b32 s80, s80, s14
	s_mul_i32 s81, s80, 0xc00
	s_add_i32 s85, s82, 0xc000
	s_mov_b32 m0, s85
	s_add_i32 s85, s82, 0x12000
	buffer_load_dwordx4 v154, s[72:75], s81 offen lds
	s_mov_b32 m0, s85
	s_add_i32 s85, s82, 0xe000
	buffer_load_dwordx4 v155, s[72:75], s81 offen lds
	s_mov_b32 m0, s85
	s_add_i32 s81, s81, 0x18000
	buffer_load_dwordx4 v154, s[72:75], s81 offen lds
	s_lshl_b32 s81, s84, 11
	s_add_i32 s85, s82, 0x0
	s_mov_b32 m0, s85
	s_add_i32 s85, s82, 0x2000
	buffer_load_dwordx4 v196, s[76:79], s81 offen lds
	s_mov_b32 m0, s85
	s_add_i32 s81, s81, 0x10000
	buffer_load_dwordx4 v196, s[76:79], s81 offen lds
	s_mov_b32 s83, s80
	ds_read_b128 v[64:67], v180 offset:32768
	ds_read_b128 v[68:71], v180 offset:40960
	ds_read_b128 v[222:225], v181 offset:32768
	ds_read_b128 v[226:229], v181 offset:40960
	ds_read_b128 v[230:233], v182 offset:32768
	ds_read_b128 v[234:237], v182 offset:40960
	ds_read_b128 v[238:241], v183 offset:32768
	ds_read_b128 v[242:245], v183 offset:40960
	v_exp_f32_e32 v164, v215
	v_add_f32_e32 v215, 0, v128
	s_waitcnt lgkmcnt(7)
	v_mfma_f32_32x32x16_bf16 v[80:95], v[64:67], v[124:127], 0
	v_add_f32_e32 v215, v198, v215
	v_add_f32_e32 v215, v129, v215
	v_add_f32_e32 v215, v163, v215
	v_add_f32_e32 v215, v130, v215
	v_add_f32_e32 v215, v162, v215
	v_add_f32_e32 v215, v131, v215
	v_add_f32_e32 v215, v161, v215
	s_waitcnt lgkmcnt(6)
	v_mfma_f32_32x32x16_bf16 v[64:79], v[68:71], v[124:127], 0
	v_add_f32_e32 v215, v132, v215
	v_add_f32_e32 v215, v139, v215
	v_add_f32_e32 v215, v133, v215
	v_add_f32_e32 v215, v138, v215
	v_add_f32_e32 v215, v134, v215
	v_exp_f32_e32 v165, v216
	v_add_f32_e32 v215, v137, v215
	s_waitcnt lgkmcnt(5)
	v_mfma_f32_32x32x16_bf16 v[80:95], v[222:225], v[120:123], v[80:95]
	v_exp_f32_e32 v217, v217
	v_add_f32_e32 v215, v135, v215
	v_exp_f32_e32 v218, v218
	v_add_f32_e32 v215, v136, v215
	v_exp_f32_e32 v219, v219
	v_add_f32_e32 v215, v164, v215
	v_exp_f32_e32 v208, v208
	s_waitcnt lgkmcnt(4)
	v_mfma_f32_32x32x16_bf16 v[64:79], v[226:229], v[120:123], v[64:79]
	ds_read_b128 v[222:225], v184 offset:32768
	ds_read_b128 v[226:229], v184 offset:40960
	v_add_f32_e32 v215, v165, v215
	v_exp_f32_e32 v209, v209
	v_add_f32_e32 v215, v217, v215
	v_exp_f32_e32 v210, v210
	v_add_f32_e32 v215, v218, v215
	v_exp_f32_e32 v211, v211
	s_waitcnt lgkmcnt(5)
	v_mfma_f32_32x32x16_bf16 v[80:95], v[230:233], v[116:119], v[80:95]
	v_add_f32_e32 v215, v219, v215
	v_exp_f32_e32 v212, v212
	v_add_f32_e32 v215, v208, v215
	v_exp_f32_e32 v213, v213
	v_add_f32_e32 v215, v209, v215
	v_exp_f32_e32 v214, v214
	v_add_f32_e32 v215, v210, v215
	s_waitcnt lgkmcnt(4)
	v_mfma_f32_32x32x16_bf16 v[64:79], v[234:237], v[116:119], v[64:79]
	ds_read_b128 v[230:233], v185 offset:32768
	ds_read_b128 v[234:237], v185 offset:40960
	v_exp_f32_e32 v207, v207
	v_add_f32_e32 v215, v211, v215
	v_exp_f32_e32 v220, v220
	v_add_f32_e32 v215, v212, v215
	v_exp_f32_e32 v221, v221
	v_add_f32_e32 v215, v213, v215
	s_waitcnt lgkmcnt(5)
	v_mfma_f32_32x32x16_bf16 v[80:95], v[238:241], v[112:115], v[80:95]
	v_exp_f32_e32 v205, v205
	v_add_f32_e32 v215, v214, v215
	v_add_f32_e32 v215, v207, v215
	v_add_f32_e32 v215, v220, v215
	v_add_f32_e32 v215, v221, v215
	v_add_f32_e32 v215, v205, v215
	v_mov_b32_e32 v216, v215
	s_waitcnt lgkmcnt(4)
	v_mfma_f32_32x32x16_bf16 v[64:79], v[242:245], v[112:115], v[64:79]
	ds_read_b128 v[238:241], v186 offset:32768
	ds_read_b128 v[242:245], v186 offset:40960
	v_permlane32_swap_b32_e32 v215, v216
	v_cvt_pk_bf16_f32 v128, v128, v198
	v_cvt_pk_bf16_f32 v129, v129, v163
	v_cvt_pk_bf16_f32 v130, v130, v162
	v_cvt_pk_bf16_f32 v131, v131, v161
	s_waitcnt lgkmcnt(5)
	v_mfma_f32_32x32x16_bf16 v[80:95], v[222:225], v[108:111], v[80:95]
	v_cvt_pk_bf16_f32 v132, v132, v139
	v_cvt_pk_bf16_f32 v133, v133, v138
	v_cvt_pk_bf16_f32 v134, v134, v137
	v_cvt_pk_bf16_f32 v135, v135, v136
	v_cvt_pk_bf16_f32 v136, v164, v165
	v_cvt_pk_bf16_f32 v137, v217, v218
	v_cvt_pk_bf16_f32 v138, v219, v208
	s_waitcnt lgkmcnt(4)
	v_mfma_f32_32x32x16_bf16 v[64:79], v[226:229], v[108:111], v[64:79]
	ds_read_b128 v[222:225], v187 offset:32768
	ds_read_b128 v[226:229], v187 offset:40960
	v_cvt_pk_bf16_f32 v139, v209, v210
	v_cvt_pk_bf16_f32 v208, v211, v212
	v_cvt_pk_bf16_f32 v209, v213, v214
	v_cvt_pk_bf16_f32 v210, v207, v220
	v_cvt_pk_bf16_f32 v211, v221, v205
	v_permlane32_swap_b32_e32 v128, v130
	s_waitcnt lgkmcnt(5)
	v_mfma_f32_32x32x16_bf16 v[80:95], v[230:233], v[104:107], v[80:95]
	v_permlane32_swap_b32_e32 v129, v131
	v_permlane32_swap_b32_e32 v132, v134
	v_permlane32_swap_b32_e32 v133, v135
	v_permlane32_swap_b32_e32 v136, v138
	s_waitcnt lgkmcnt(4)
	v_mfma_f32_32x32x16_bf16 v[64:79], v[234:237], v[104:107], v[64:79]
	ds_read_b128 v[230:233], v191
	ds_read_b128 v[234:237], v191 offset:4096
	v_permlane32_swap_b32_e32 v137, v139
	v_permlane32_swap_b32_e32 v208, v210
	v_permlane32_swap_b32_e32 v209, v211
	s_waitcnt lgkmcnt(5)
	v_mfma_f32_32x32x16_bf16 v[80:95], v[238:241], v[100:103], v[80:95]
	s_waitcnt lgkmcnt(4)
	v_mfma_f32_32x32x16_bf16 v[64:79], v[242:245], v[100:103], v[64:79]
	ds_read_b128 v[238:241], v192
	ds_read_b128 v[242:245], v192 offset:4096
	s_waitcnt lgkmcnt(5)
	v_mfma_f32_32x32x16_bf16 v[80:95], v[222:225], v[96:99], v[80:95]
	s_waitcnt lgkmcnt(4)
	v_mfma_f32_32x32x16_bf16 v[64:79], v[226:229], v[96:99], v[64:79]
	ds_read_b128 v[222:225], v193
	ds_read_b128 v[226:229], v193 offset:4096
	s_waitcnt lgkmcnt(5)
	v_mfma_f32_32x32x16_bf16 v[80:95], v[230:233], v[142:145], v[80:95]
	s_waitcnt lgkmcnt(4)
	v_mfma_f32_32x32x16_bf16 v[64:79], v[234:237], v[142:145], v[64:79]
	ds_read_b128 v[230:233], v194
	ds_read_b128 v[234:237], v194 offset:4096
	s_waitcnt lgkmcnt(5)
	v_mfma_f32_32x32x16_bf16 v[80:95], v[238:241], v[146:149], v[80:95]
	s_waitcnt lgkmcnt(4)
	v_mfma_f32_32x32x16_bf16 v[64:79], v[242:245], v[146:149], v[64:79]
	s_waitcnt lgkmcnt(3)
	v_mfma_f32_32x32x16_bf16 v[80:95], v[222:225], v[150:153], v[80:95]
	s_waitcnt lgkmcnt(2)
	v_mfma_f32_32x32x16_bf16 v[64:79], v[226:229], v[150:153], v[64:79]
	s_waitcnt lgkmcnt(1)
	v_mfma_f32_32x32x16_bf16 v[80:95], v[230:233], v[156:159], v[80:95]
	s_waitcnt lgkmcnt(0)
	v_mfma_f32_32x32x16_bf16 v[64:79], v[234:237], v[156:159], v[64:79]
	ds_read_b64_tr_b16 v[238:239], v174 offset:0
	ds_read_b64_tr_b16 v[240:241], v174 offset:0x800
	ds_read_b64_tr_b16 v[242:243], v174 offset:0x1000
	ds_read_b64_tr_b16 v[244:245], v174 offset:0x1800
	ds_read_b64_tr_b16 v[246:247], v174 offset:0x2000
	ds_read_b64_tr_b16 v[248:249], v174 offset:0x2800
	ds_read_b64_tr_b16 v[250:251], v174 offset:0x3000
	ds_read_b64_tr_b16 v[252:253], v174 offset:0x3800
	s_nop 3
	v_max_f32_e32 v161, v81, v81
	v_max_f32_e32 v162, v80, v80
	v_max_f32_e32 v161, v162, v161
	v_max3_f32 v161, v161, v82, v83
	v_max3_f32 v161, v161, v84, v85
	v_max3_f32 v161, v161, v86, v87
	v_max3_f32 v161, v161, v88, v89
	v_max3_f32 v161, v161, v90, v91
	v_max3_f32 v161, v161, v92, v93
	v_max3_f32 v161, v161, v94, v95
	s_waitcnt lgkmcnt(0)
	v_mfma_f32_32x32x16_bf16 v[0:15], v[128:131], v[238:241], v[0:15]
	ds_read_b64_tr_b16 v[238:239], v174 offset:0x200
	ds_read_b64_tr_b16 v[240:241], v174 offset:0xa00
	v_max3_f32 v161, v161, v64, v65
	v_max3_f32 v161, v161, v66, v67
	v_max3_f32 v161, v161, v68, v69
	v_mfma_f32_32x32x16_bf16 v[0:15], v[132:135], v[242:245], v[0:15]
	ds_read_b64_tr_b16 v[242:243], v174 offset:0x1200
	ds_read_b64_tr_b16 v[244:245], v174 offset:0x1a00
	v_max3_f32 v161, v161, v70, v71
	v_max3_f32 v161, v161, v72, v73
	v_max3_f32 v161, v161, v74, v75
	v_mfma_f32_32x32x16_bf16 v[0:15], v[136:139], v[246:249], v[0:15]
	ds_read_b64_tr_b16 v[246:247], v174 offset:0x2200
	ds_read_b64_tr_b16 v[248:249], v174 offset:0x2a00
	ds_read_b64_tr_b16 v[162:163], v174 offset:0x3200
	ds_read_b64_tr_b16 v[164:165], v174 offset:0x3a00
	v_max3_f32 v161, v161, v76, v77
	v_max3_f32 v161, v161, v78, v79
	v_mov_b32_e32 v198, v161
	v_mfma_f32_32x32x16_bf16 v[0:15], v[208:211], v[250:253], v[0:15]
	v_max_f32_e32 v205, v160, v160
	v_permlane32_swap_b32_e32 v161, v198
	v_max_f32_e32 v198, v198, v198
	v_max_f32_e32 v161, v161, v161
	v_max_f32_e32 v161, v161, v198
	s_waitcnt lgkmcnt(0)
	v_mfma_f32_32x32x16_bf16 v[32:47], v[128:131], v[238:241], v[32:47]
	ds_read_b64_tr_b16 v[238:239], v174 offset:0x400
	ds_read_b64_tr_b16 v[240:241], v174 offset:0xc00
	v_sub_f32_e32 v198, v161, v160
	v_max_f32_e32 v161, v205, v161
	v_sub_f32_e32 v205, v160, v161
	v_mul_f32_e32 v205, 0x3dd53b94, v205
	v_exp_f32_e32 v205, v205
	v_mfma_f32_32x32x16_bf16 v[32:47], v[132:135], v[242:245], v[32:47]
	ds_read_b64_tr_b16 v[242:243], v174 offset:0x1400
	ds_read_b64_tr_b16 v[244:245], v174 offset:0x1c00
	v_cmp_ge_f32_e32 vcc, s46, v198
	s_cmp_eq_u64 vcc, exec
	s_cselect_b64 s[6:7], -1, 0
	v_cndmask_b32_e64 v205, v205, 1.0, s[6:7]
	v_cndmask_b32_e64 v198, v161, v160, s[6:7]
	v_mul_f32_e32 v236, 0xbdd53b94, v198
	v_mov_b32_e32 v237, v236
	v_cmp_gt_f32_e32 vcc, 1.0, v205
	v_mfma_f32_32x32x16_bf16 v[32:47], v[136:139], v[246:249], v[32:47]
	ds_read_b64_tr_b16 v[246:247], v174 offset:0x2400
	ds_read_b64_tr_b16 v[248:249], v174 offset:0x2c00
	ds_read_b64_tr_b16 v[250:251], v174 offset:0x3400
	ds_read_b64_tr_b16 v[252:253], v174 offset:0x3c00
	v_fmamk_f32 v80, v80, 0x3dd53b94, v236
	v_fmamk_f32 v81, v81, 0x3dd53b94, v236
	v_fmamk_f32 v82, v82, 0x3dd53b94, v236
	v_fmamk_f32 v83, v83, 0x3dd53b94, v236
	v_mfma_f32_32x32x16_bf16 v[32:47], v[208:211], v[162:165], v[32:47]
	v_fmamk_f32 v84, v84, 0x3dd53b94, v236
	v_fmamk_f32 v85, v85, 0x3dd53b94, v236
	v_fmamk_f32 v86, v86, 0x3dd53b94, v236
	v_fmamk_f32 v87, v87, 0x3dd53b94, v236
	s_waitcnt lgkmcnt(0)
	v_mfma_f32_32x32x16_bf16 v[16:31], v[128:131], v[238:241], v[16:31]
	ds_read_b64_tr_b16 v[162:163], v174 offset:0x600
	ds_read_b64_tr_b16 v[164:165], v174 offset:0xe00
	ds_read_b64_tr_b16 v[238:239], v174 offset:0x1600
	ds_read_b64_tr_b16 v[240:241], v174 offset:0x1e00
	v_fmamk_f32 v88, v88, 0x3dd53b94, v236
	v_fmamk_f32 v89, v89, 0x3dd53b94, v236
	v_fmamk_f32 v90, v90, 0x3dd53b94, v236
	v_fmamk_f32 v91, v91, 0x3dd53b94, v236
	v_mfma_f32_32x32x16_bf16 v[16:31], v[132:135], v[242:245], v[16:31]
	ds_read_b64_tr_b16 v[242:243], v174 offset:0x2600
	ds_read_b64_tr_b16 v[244:245], v174 offset:0x2e00
	v_fmamk_f32 v92, v92, 0x3dd53b94, v236
	v_fmamk_f32 v93, v93, 0x3dd53b94, v236
	v_fmamk_f32 v94, v94, 0x3dd53b94, v236
	v_fmamk_f32 v95, v95, 0x3dd53b94, v236
	v_mfma_f32_32x32x16_bf16 v[16:31], v[136:139], v[246:249], v[16:31]
	ds_read_b64_tr_b16 v[246:247], v174 offset:0x3600
	ds_read_b64_tr_b16 v[248:249], v174 offset:0x3e00
	v_exp_f32_e32 v222, v80
	v_exp_f32_e32 v224, v81
	v_exp_f32_e32 v220, v82
	v_mfma_f32_32x32x16_bf16 v[16:31], v[208:211], v[250:253], v[16:31]
	v_exp_f32_e32 v223, v83
	v_exp_f32_e32 v219, v84
	v_exp_f32_e32 v221, v85
	s_waitcnt lgkmcnt(0)
	v_mfma_f32_32x32x16_bf16 v[48:63], v[128:131], v[162:165], v[48:63]
	v_exp_f32_e32 v217, v86
	v_exp_f32_e32 v218, v87
	v_exp_f32_e32 v212, v88
	v_pk_fma_f32 v[130:131], v[70:71], s[26:27], v[236:237] op_sel_hi:[1,0,0]
	v_pk_fma_f32 v[128:129], v[72:73], s[26:27], v[236:237] op_sel_hi:[1,0,0]
	v_mfma_f32_32x32x16_bf16 v[48:63], v[132:135], v[238:241], v[48:63]
	v_exp_f32_e32 v214, v89
	v_exp_f32_e32 v213, v91
	v_exp_f32_e32 v207, v94
	v_pk_fma_f32 v[132:133], v[68:69], s[26:27], v[236:237] op_sel_hi:[1,0,0]
	v_pk_fma_f32 v[134:135], v[78:79], s[26:27], v[236:237] op_sel_hi:[1,0,0]
	v_mfma_f32_32x32x16_bf16 v[48:63], v[136:139], v[242:245], v[48:63]
	v_pk_fma_f32 v[138:139], v[64:65], s[26:27], v[236:237] op_sel_hi:[1,0,0]
	v_pk_fma_f32 v[136:137], v[66:67], s[26:27], v[236:237] op_sel_hi:[1,0,0]
	v_pk_fma_f32 v[162:163], v[74:75], s[26:27], v[236:237] op_sel_hi:[1,0,0]
	v_pk_fma_f32 v[160:161], v[76:77], s[26:27], v[236:237] op_sel_hi:[1,0,0]
	v_mfma_f32_32x32x16_bf16 v[48:63], v[208:211], v[246:249], v[48:63]
	v_exp_f32_e32 v211, v90
	v_exp_f32_e32 v208, v92
	v_exp_f32_e32 v210, v93
	v_exp_f32_e32 v209, v95
	v_add_f32_e32 v64, v203, v204
	v_fmac_f32_e32 v64, v197, v140
	v_add_f32_e32 v140, v215, v216
	s_addk_i32 s13, 0x80
	s_addk_i32 s14, 0x80
	v_fmac_f32_e32 v140, v64, v206
	s_cbranch_vccz .LBB0_2020
	s_and_saveexec_b64 s[10:11], s[4:5]
	ds_write_b32 v189, v205 offset:128
	s_or_b64 exec, exec, s[10:11]
	s_waitcnt lgkmcnt(0)
	v_add_u32_e32 v164, s12, v169
	ds_read_b128 v[238:241], v164 offset:224
	ds_read_b128 v[242:245], v164 offset:192
	ds_read_b128 v[246:249], v164 offset:160
	ds_read_b128 v[250:253], v164 offset:128
	s_waitcnt lgkmcnt(3)
	v_pk_mul_f32 v[12:13], v[12:13], v[238:239]
	s_waitcnt lgkmcnt(2)
	v_pk_mul_f32 v[8:9], v[8:9], v[242:243]
	s_waitcnt lgkmcnt(1)
	v_pk_mul_f32 v[4:5], v[4:5], v[246:247]
	v_pk_mul_f32 v[14:15], v[14:15], v[240:241]
	v_pk_mul_f32 v[10:11], v[10:11], v[244:245]
	v_pk_mul_f32 v[6:7], v[6:7], v[248:249]
	s_waitcnt lgkmcnt(0)
	v_pk_mul_f32 v[2:3], v[2:3], v[252:253]
	v_pk_mul_f32 v[0:1], v[0:1], v[250:251]
	v_pk_mul_f32 v[44:45], v[44:45], v[238:239]
	v_pk_mul_f32 v[40:41], v[40:41], v[242:243]
	v_pk_mul_f32 v[36:37], v[36:37], v[246:247]
	v_pk_mul_f32 v[46:47], v[46:47], v[240:241]
	v_pk_mul_f32 v[42:43], v[42:43], v[244:245]
	v_pk_mul_f32 v[38:39], v[38:39], v[248:249]
	v_pk_mul_f32 v[34:35], v[34:35], v[252:253]
	v_pk_mul_f32 v[32:33], v[32:33], v[250:251]
	v_pk_mul_f32 v[28:29], v[28:29], v[238:239]
	v_pk_mul_f32 v[24:25], v[24:25], v[242:243]
	v_pk_mul_f32 v[20:21], v[20:21], v[246:247]
	v_pk_mul_f32 v[30:31], v[30:31], v[240:241]
	v_pk_mul_f32 v[26:27], v[26:27], v[244:245]
	v_pk_mul_f32 v[22:23], v[22:23], v[248:249]
	v_pk_mul_f32 v[18:19], v[18:19], v[252:253]
	v_pk_mul_f32 v[16:17], v[16:17], v[250:251]
	v_pk_mul_f32 v[60:61], v[60:61], v[238:239]
	v_pk_mul_f32 v[56:57], v[56:57], v[242:243]
	v_pk_mul_f32 v[52:53], v[52:53], v[246:247]
	v_pk_mul_f32 v[62:63], v[62:63], v[240:241]
	v_pk_mul_f32 v[58:59], v[58:59], v[244:245]
	v_pk_mul_f32 v[54:55], v[54:55], v[248:249]
	v_pk_mul_f32 v[50:51], v[50:51], v[252:253]
	v_pk_mul_f32 v[48:49], v[48:49], v[250:251]

.LBB0_2022:
	s_lshl_b32 s81, s83, 11
	s_add_i32 s85, s82, 0x4000
	s_mov_b32 m0, s85
	s_add_i32 s85, s82, 0x6000
	buffer_load_dwordx4 v196, s[76:79], s81 offen lds
	s_mov_b32 m0, s85
	s_add_i32 s81, s81, 0x10000
	buffer_load_dwordx4 v196, s[76:79], s81 offen lds
	ds_read_b128 v[64:67], v180 offset:49152
	ds_read_b128 v[68:71], v180 offset:57344
	v_exp_f32_e32 v138, v138
	v_exp_f32_e32 v139, v139
	v_exp_f32_e32 v136, v136
	s_waitcnt lgkmcnt(1)
	v_mfma_f32_32x32x16_bf16 v[80:95], v[64:67], v[124:127], 0
	v_exp_f32_e32 v137, v137
	v_exp_f32_e32 v132, v132
	v_exp_f32_e32 v128, v128
	v_exp_f32_e32 v129, v129
	s_waitcnt lgkmcnt(0)
	v_mfma_f32_32x32x16_bf16 v[64:79], v[68:71], v[124:127], 0
	ds_read_b128 v[124:127], v181 offset:49152
	ds_read_b128 v[154:157], v181 offset:57344
	s_waitcnt lgkmcnt(1)
	v_mfma_f32_32x32x16_bf16 v[80:95], v[124:127], v[120:123], v[80:95]
	s_waitcnt lgkmcnt(0)
	v_mfma_f32_32x32x16_bf16 v[64:79], v[154:157], v[120:123], v[64:79]
	ds_read_b128 v[120:123], v182 offset:49152
	ds_read_b128 v[124:127], v182 offset:57344
	s_waitcnt lgkmcnt(1)
	v_mfma_f32_32x32x16_bf16 v[80:95], v[120:123], v[116:119], v[80:95]
	s_waitcnt lgkmcnt(0)
	v_mfma_f32_32x32x16_bf16 v[64:79], v[124:127], v[116:119], v[64:79]
	ds_read_b128 v[116:119], v183 offset:49152
	ds_read_b128 v[120:123], v183 offset:57344
	s_waitcnt lgkmcnt(1)
	v_mfma_f32_32x32x16_bf16 v[80:95], v[116:119], v[112:115], v[80:95]
	s_waitcnt lgkmcnt(0)
	v_mfma_f32_32x32x16_bf16 v[64:79], v[120:123], v[112:115], v[64:79]
	ds_read_b128 v[112:115], v184 offset:49152
	ds_read_b128 v[116:119], v184 offset:57344
	s_waitcnt lgkmcnt(1)
	v_mfma_f32_32x32x16_bf16 v[80:95], v[112:115], v[108:111], v[80:95]
	ds_read_b128 v[112:115], v185 offset:49152
	s_waitcnt lgkmcnt(1)
	v_mfma_f32_32x32x16_bf16 v[64:79], v[116:119], v[108:111], v[64:79]
	ds_read_b128 v[108:111], v185 offset:57344
	ds_read_b128 v[116:119], v186 offset:49152
	ds_read_b128 v[120:123], v186 offset:57344
	ds_read_b128 v[124:127], v187 offset:49152
	ds_read_b128 v[154:157], v187 offset:57344
	ds_read_b128 v[192:195], v199
	ds_read_b128 v[226:229], v199 offset:4096
	s_waitcnt lgkmcnt(7)
	v_mfma_f32_32x32x16_bf16 v[80:95], v[112:115], v[104:107], v[80:95]
	ds_read_b128 v[112:115], v200
	ds_read_b128 v[230:233], v200 offset:4096
	ds_read_b128 v[234:237], v190
	ds_read_b128 v[238:241], v190 offset:1024
	ds_read_b128 v[242:245], v201
	ds_read_b128 v[246:249], v201 offset:4096
	ds_read_b128 v[250:253], v202
	ds_read_b128 v[200:203], v202 offset:4096
	s_waitcnt lgkmcnt(14)
	v_mfma_f32_32x32x16_bf16 v[64:79], v[108:111], v[104:107], v[64:79]
	ds_read_b128 v[104:107], v190 offset:2048
	ds_read_b128 v[108:111], v190 offset:3072
	s_waitcnt lgkmcnt(14)
	v_mfma_f32_32x32x16_bf16 v[80:95], v[116:119], v[100:103], v[80:95]
	v_exp_f32_e32 v118, v133
	v_exp_f32_e32 v119, v130
	v_exp_f32_e32 v130, v131
	v_exp_f32_e32 v131, v162
	v_exp_f32_e32 v133, v163
	v_cvt_pk_bf16_f32 v116, v138, v139
	v_cvt_pk_bf16_f32 v117, v136, v137
	v_mfma_f32_32x32x16_bf16 v[64:79], v[120:123], v[100:103], v[64:79]
	v_add_f32_e32 v100, 0, v222
	v_add_f32_e32 v100, v224, v100
	v_add_f32_e32 v100, v220, v100
	v_add_f32_e32 v100, v223, v100
	v_add_f32_e32 v100, v219, v100
	v_add_f32_e32 v100, v221, v100
	v_add_f32_e32 v100, v217, v100
	s_waitcnt lgkmcnt(13)
	v_mfma_f32_32x32x16_bf16 v[80:95], v[124:127], v[96:99], v[80:95]
	v_add_f32_e32 v100, v218, v100
	v_add_f32_e32 v100, v212, v100
	v_add_f32_e32 v100, v214, v100
	v_exp_f32_e32 v120, v160
	v_exp_f32_e32 v121, v161
	v_exp_f32_e32 v122, v134
	v_exp_f32_e32 v123, v135
	s_waitcnt lgkmcnt(12)
	v_mfma_f32_32x32x16_bf16 v[64:79], v[154:157], v[96:99], v[64:79]
	v_add_f32_e32 v96, v211, v100
	v_add_f32_e32 v96, v213, v96
	v_add_f32_e32 v96, v208, v96
	v_add_f32_e32 v96, v210, v96
	v_add_f32_e32 v96, v207, v96
	v_add_f32_e32 v96, v209, v96
	v_add_f32_e32 v96, v138, v96
	s_waitcnt lgkmcnt(7)
	v_mfma_f32_32x32x16_bf16 v[80:95], v[192:195], v[234:237], v[80:95]
	v_add_f32_e32 v96, v139, v96
	v_add_f32_e32 v96, v136, v96
	v_add_f32_e32 v96, v137, v96
	v_add_f32_e32 v96, v132, v96
	v_add_f32_e32 v96, v118, v96
	v_add_f32_e32 v96, v119, v96
	v_add_f32_e32 v96, v130, v96
	v_mfma_f32_32x32x16_bf16 v[64:79], v[226:229], v[234:237], v[64:79]
	v_add_f32_e32 v96, v128, v96
	v_add_f32_e32 v96, v129, v96
	v_add_f32_e32 v96, v131, v96
	v_add_f32_e32 v96, v133, v96
	v_add_f32_e32 v96, v120, v96
	v_add_f32_e32 v96, v121, v96
	v_add_f32_e32 v96, v122, v96
	s_waitcnt lgkmcnt(6)
	v_mfma_f32_32x32x16_bf16 v[80:95], v[112:115], v[238:241], v[80:95]
	v_add_f32_e32 v96, v123, v96
	v_mov_b32_e32 v97, v96
	s_nop 1
	v_permlane32_swap_b32_e32 v96, v97
	v_cvt_pk_bf16_f32 v100, v222, v224
	v_cvt_pk_bf16_f32 v101, v220, v223
	v_cvt_pk_bf16_f32 v102, v219, v221
	v_mfma_f32_32x32x16_bf16 v[64:79], v[230:233], v[238:241], v[64:79]
	v_cvt_pk_bf16_f32 v103, v217, v218
	v_cvt_pk_bf16_f32 v112, v212, v214
	v_cvt_pk_bf16_f32 v113, v211, v213
	v_cvt_pk_bf16_f32 v114, v208, v210
	v_cvt_pk_bf16_f32 v115, v207, v209
	v_cvt_pk_bf16_f32 v118, v132, v118
	v_cvt_pk_bf16_f32 v119, v119, v130
	s_waitcnt lgkmcnt(1)
	v_mfma_f32_32x32x16_bf16 v[80:95], v[242:245], v[104:107], v[80:95]
	v_permlane32_swap_b32_e32 v100, v102
	v_permlane32_swap_b32_e32 v101, v103
	v_permlane32_swap_b32_e32 v112, v114
	v_permlane32_swap_b32_e32 v113, v115
	v_mfma_f32_32x32x16_bf16 v[64:79], v[246:249], v[104:107], v[64:79]
	v_cvt_pk_bf16_f32 v104, v128, v129
	v_cvt_pk_bf16_f32 v105, v131, v133
	v_cvt_pk_bf16_f32 v106, v120, v121
	v_cvt_pk_bf16_f32 v107, v122, v123
	v_permlane32_swap_b32_e32 v116, v118
	v_permlane32_swap_b32_e32 v117, v119
	s_waitcnt lgkmcnt(0)
	v_mfma_f32_32x32x16_bf16 v[80:95], v[250:253], v[108:111], v[80:95]
	v_permlane32_swap_b32_e32 v104, v106
	v_permlane32_swap_b32_e32 v105, v107
	v_mfma_f32_32x32x16_bf16 v[64:79], v[200:203], v[108:111], v[64:79]
	ds_read_b64_tr_b16 v[108:109], v167 offset:0
	ds_read_b64_tr_b16 v[110:111], v167 offset:0x800
	ds_read_b64_tr_b16 v[120:121], v167 offset:0x1000
	ds_read_b64_tr_b16 v[122:123], v167 offset:0x1800
	ds_read_b64_tr_b16 v[124:125], v167 offset:0x2000
	ds_read_b64_tr_b16 v[126:127], v167 offset:0x2800
	ds_read_b64_tr_b16 v[128:129], v167 offset:0x3000
	ds_read_b64_tr_b16 v[130:131], v167 offset:0x3800
	s_nop 8
	v_max_f32_e32 v98, v81, v81
	v_max_f32_e32 v99, v80, v80
	v_max_f32_e32 v98, v99, v98
	v_max3_f32 v98, v98, v82, v83
	v_max3_f32 v98, v98, v84, v85
	v_max3_f32 v98, v98, v86, v87
	v_max3_f32 v98, v98, v88, v89
	v_max3_f32 v98, v98, v90, v91
	v_max3_f32 v98, v98, v92, v93
	v_max3_f32 v98, v98, v94, v95
	s_waitcnt lgkmcnt(0)
	v_mfma_f32_32x32x16_bf16 v[0:15], v[100:103], v[108:111], v[0:15]
	ds_read_b64_tr_b16 v[108:109], v167 offset:0x200
	ds_read_b64_tr_b16 v[110:111], v167 offset:0xa00
	v_mfma_f32_32x32x16_bf16 v[0:15], v[112:115], v[120:123], v[0:15]
	ds_read_b64_tr_b16 v[120:121], v167 offset:0x1200
	ds_read_b64_tr_b16 v[122:123], v167 offset:0x1a00
	v_mfma_f32_32x32x16_bf16 v[0:15], v[116:119], v[124:127], v[0:15]
	ds_read_b64_tr_b16 v[124:125], v167 offset:0x2200
	ds_read_b64_tr_b16 v[126:127], v167 offset:0x2a00
	ds_read_b64_tr_b16 v[132:133], v167 offset:0x3200
	ds_read_b64_tr_b16 v[134:135], v167 offset:0x3a00
	v_mfma_f32_32x32x16_bf16 v[0:15], v[104:107], v[128:131], v[0:15]
	v_max3_f32 v98, v98, v64, v65
	v_max3_f32 v98, v98, v66, v67
	v_max3_f32 v98, v98, v68, v69
	v_max3_f32 v98, v98, v70, v71
	v_max3_f32 v98, v98, v72, v73
	v_max3_f32 v98, v98, v74, v75
	v_max3_f32 v98, v98, v76, v77
	v_max3_f32 v98, v98, v78, v79
	v_mov_b32_e32 v99, v98
	s_nop 1
	v_permlane32_swap_b32_e32 v98, v99
	v_max_f32_e32 v99, v99, v99
	v_max_f32_e32 v98, v98, v98
	v_max_f32_e32 v98, v98, v99
	v_max_f32_e32 v99, v198, v198
	v_max_f32_e32 v99, v99, v98
	v_sub_f32_e32 v128, v98, v198
	v_sub_f32_e32 v98, v198, v99
	v_mul_f32_e32 v98, 0x3dd53b94, v98
	v_exp_f32_e32 v98, v98
	v_cmp_ge_f32_e32 vcc, s46, v128
	s_cmp_eq_u64 vcc, exec
	s_cselect_b64 s[6:7], -1, 0
	v_cndmask_b32_e64 v98, v98, 1.0, s[6:7]
	s_waitcnt lgkmcnt(0)
	v_mfma_f32_32x32x16_bf16 v[32:47], v[100:103], v[108:111], v[32:47]
	ds_read_b64_tr_b16 v[108:109], v167 offset:0x400
	ds_read_b64_tr_b16 v[110:111], v167 offset:0xc00
	v_mfma_f32_32x32x16_bf16 v[32:47], v[112:115], v[120:123], v[32:47]
	ds_read_b64_tr_b16 v[120:121], v167 offset:0x1400
	ds_read_b64_tr_b16 v[122:123], v167 offset:0x1c00
	v_mfma_f32_32x32x16_bf16 v[32:47], v[116:119], v[124:127], v[32:47]
	ds_read_b64_tr_b16 v[124:125], v167 offset:0x2400
	ds_read_b64_tr_b16 v[126:127], v167 offset:0x2c00
	ds_read_b64_tr_b16 v[128:129], v167 offset:0x3400
	ds_read_b64_tr_b16 v[130:131], v167 offset:0x3c00
	v_mfma_f32_32x32x16_bf16 v[32:47], v[104:107], v[132:135], v[32:47]
	s_waitcnt lgkmcnt(0)
	v_mfma_f32_32x32x16_bf16 v[16:31], v[100:103], v[108:111], v[16:31]
	ds_read_b64_tr_b16 v[108:109], v167 offset:0x600
	ds_read_b64_tr_b16 v[110:111], v167 offset:0xe00
	v_mfma_f32_32x32x16_bf16 v[16:31], v[112:115], v[120:123], v[16:31]
	ds_read_b64_tr_b16 v[120:121], v167 offset:0x1600
	ds_read_b64_tr_b16 v[122:123], v167 offset:0x1e00
	v_mfma_f32_32x32x16_bf16 v[16:31], v[116:119], v[124:127], v[16:31]
	ds_read_b64_tr_b16 v[124:125], v167 offset:0x2600
	ds_read_b64_tr_b16 v[126:127], v167 offset:0x2e00
	ds_read_b64_tr_b16 v[132:133], v167 offset:0x3600
	ds_read_b64_tr_b16 v[134:135], v167 offset:0x3e00
	v_mfma_f32_32x32x16_bf16 v[16:31], v[104:107], v[128:131], v[16:31]
	s_waitcnt lgkmcnt(0)
	v_mfma_f32_32x32x16_bf16 v[48:63], v[100:103], v[108:111], v[48:63]
	v_cmp_gt_f32_e32 vcc, 1.0, v98
	s_waitcnt vmcnt(0)
	s_barrier
	v_mfma_f32_32x32x16_bf16 v[48:63], v[112:115], v[120:123], v[48:63]
	v_mfma_f32_32x32x16_bf16 v[48:63], v[116:119], v[124:127], v[48:63]
	v_mfma_f32_32x32x16_bf16 v[48:63], v[104:107], v[132:135], v[48:63]
	s_cbranch_vccz .LBB0_2026
	s_and_saveexec_b64 s[10:11], s[4:5]
	ds_write_b32 v189, v98 offset:128
	s_or_b64 exec, exec, s[10:11]
	s_waitcnt lgkmcnt(0)
	v_add_u32_e32 v112, s12, v169
	ds_read_b128 v[100:103], v112 offset:224
	ds_read_b128 v[104:107], v112 offset:192
	ds_read_b128 v[108:111], v112 offset:160
	ds_read_b128 v[112:115], v112 offset:128
	s_waitcnt lgkmcnt(3)
	v_pk_mul_f32 v[12:13], v[12:13], v[100:101]
	s_waitcnt lgkmcnt(2)
	v_pk_mul_f32 v[8:9], v[8:9], v[104:105]
	s_waitcnt lgkmcnt(1)
	v_pk_mul_f32 v[4:5], v[4:5], v[108:109]
	v_pk_mul_f32 v[14:15], v[14:15], v[102:103]
	v_pk_mul_f32 v[10:11], v[10:11], v[106:107]
	v_pk_mul_f32 v[6:7], v[6:7], v[110:111]
	s_waitcnt lgkmcnt(0)
	v_pk_mul_f32 v[2:3], v[2:3], v[114:115]
	v_pk_mul_f32 v[0:1], v[0:1], v[112:113]
	v_pk_mul_f32 v[44:45], v[44:45], v[100:101]
	v_pk_mul_f32 v[40:41], v[40:41], v[104:105]
	v_pk_mul_f32 v[36:37], v[36:37], v[108:109]
	v_pk_mul_f32 v[46:47], v[46:47], v[102:103]
	v_pk_mul_f32 v[42:43], v[42:43], v[106:107]
	v_pk_mul_f32 v[38:39], v[38:39], v[110:111]
	v_pk_mul_f32 v[34:35], v[34:35], v[114:115]
	v_pk_mul_f32 v[32:33], v[32:33], v[112:113]
	v_pk_mul_f32 v[28:29], v[28:29], v[100:101]
	v_pk_mul_f32 v[24:25], v[24:25], v[104:105]
	v_pk_mul_f32 v[20:21], v[20:21], v[108:109]
	v_pk_mul_f32 v[30:31], v[30:31], v[102:103]
	v_pk_mul_f32 v[26:27], v[26:27], v[106:107]
	v_pk_mul_f32 v[22:23], v[22:23], v[110:111]
	v_pk_mul_f32 v[18:19], v[18:19], v[114:115]
	v_pk_mul_f32 v[16:17], v[16:17], v[112:113]
	v_pk_mul_f32 v[60:61], v[60:61], v[100:101]
	v_pk_mul_f32 v[56:57], v[56:57], v[104:105]
	v_pk_mul_f32 v[52:53], v[52:53], v[108:109]
	v_pk_mul_f32 v[62:63], v[62:63], v[102:103]
	v_pk_mul_f32 v[58:59], v[58:59], v[106:107]
	v_pk_mul_f32 v[54:55], v[54:55], v[110:111]
	v_pk_mul_f32 v[50:51], v[50:51], v[114:115]
	v_pk_mul_f32 v[48:49], v[48:49], v[112:113]
